# router: the next pass's row prefetch stays in flight through the normalisation chain (first chain step waits only on LDS)
# speedup vs baseline: 1.0144x; 1.0025x over previous
; DI float bflo(unsigned u) { return __uint_as_float(u << 16); }
; DI float bfhi(unsigned u) { return __uint_as_float(u & 0xffff0000u); }
; template <bool DRY = false>
; DI void phase_ln_router(const Params& p, char* smem, int bid, int nb) {
;     ...
;     const int t = t0 + wv;
;     {
;       float v[32];
; #pragma unroll
;       for (int i = 0; i < 8; ++i) {
;         const u32x2 a = za[i];
;         v[4 * i] = bflo(a.x); v[4 * i + 1] = bfhi(a.x); v[4 * i + 2] = bflo(a.y); v[4 * i + 3] = bfhi(a.y);
;       }
;       {
;         const int tn2 = t + nb * 8;
;         const bf16_t* zr = p.z1b + (size_t)(tn2 < NTOK ? tn2 : t) * DM;
; #pragma unroll
;         for (int i = 0; i < 8; ++i) za[i] = *(const u32x2*)(zr + (i * 64 + lane) * 4);
;       }
;       float s = 0.f;
; #pragma unroll
;       for (int i = 0; i < 32; ++i) s += v[i];
;       s = wave_sum(s);
;       const float mu = s * (1.f / 2048.f);
;       float q = 0.f;
; #pragma unroll
;       for (int i = 0; i < 32; ++i) { const float d = v[i] - mu; q += d * d; }
;       q = wave_sum(q);
;       const float rs = rsqrtf(q * (1.f / 2048.f) + LN_EPS);
.LBB0_1330:
	s_waitcnt vmcnt(0)
	v_lshlrev_b32_e32 v182, 16, v174
	v_and_b32_e32 v183, 0xffff0000, v174
	v_add_f32_e32 v0, 0, v182
	v_add_f32_e32 v0, v0, v183
	v_lshlrev_b32_e32 v174, 16, v175
	v_and_b32_e32 v175, 0xffff0000, v175
	v_add_f32_e32 v0, v0, v174
	v_add_f32_e32 v0, v0, v175
	v_lshlrev_b32_e32 v184, 16, v170
	v_and_b32_e32 v185, 0xffff0000, v170
	v_add_f32_e32 v0, v0, v184
	v_add_f32_e32 v0, v0, v185
	v_lshlrev_b32_e32 v170, 16, v171
	v_and_b32_e32 v171, 0xffff0000, v171
	v_add_f32_e32 v0, v0, v170
	v_add_f32_e32 v0, v0, v171
	v_lshlrev_b32_e32 v186, 16, v168
	v_and_b32_e32 v187, 0xffff0000, v168
	v_add_f32_e32 v0, v0, v186
	v_add_f32_e32 v0, v0, v187
	v_lshlrev_b32_e32 v168, 16, v169
	v_and_b32_e32 v169, 0xffff0000, v169
	v_add_f32_e32 v0, v0, v168
	v_add_f32_e32 v0, v0, v169
	v_lshlrev_b32_e32 v188, 16, v166
	v_and_b32_e32 v189, 0xffff0000, v166
	v_add_f32_e32 v0, v0, v188
	v_add_f32_e32 v0, v0, v189
	v_lshlrev_b32_e32 v166, 16, v167
	v_and_b32_e32 v167, 0xffff0000, v167
	v_add_f32_e32 v0, v0, v166
	v_add_f32_e32 v0, v0, v167
	v_lshlrev_b32_e32 v190, 16, v180
	v_and_b32_e32 v191, 0xffff0000, v180
	v_add_f32_e32 v0, v0, v190
	v_add_f32_e32 v0, v0, v191
	v_lshlrev_b32_e32 v180, 16, v181
	v_and_b32_e32 v181, 0xffff0000, v181
	v_add_f32_e32 v0, v0, v180
	v_add_f32_e32 v0, v0, v181
	v_lshlrev_b32_e32 v192, 16, v178
	v_and_b32_e32 v193, 0xffff0000, v178
	v_add_f32_e32 v0, v0, v192
	v_add_f32_e32 v0, v0, v193
	v_lshlrev_b32_e32 v178, 16, v179
	v_and_b32_e32 v179, 0xffff0000, v179
	v_add_f32_e32 v0, v0, v178
	v_add_f32_e32 v0, v0, v179
	v_lshlrev_b32_e32 v222, 16, v176
	v_and_b32_e32 v223, 0xffff0000, v176
	v_add_f32_e32 v0, v0, v222
	v_add_f32_e32 v0, v0, v223
	v_lshlrev_b32_e32 v176, 16, v177
	v_and_b32_e32 v177, 0xffff0000, v177
	v_add_f32_e32 v0, v0, v176
	v_add_f32_e32 v0, v0, v177
	v_lshlrev_b32_e32 v224, 16, v172
	v_and_b32_e32 v225, 0xffff0000, v172
	v_add_f32_e32 v0, v0, v224
	v_add_f32_e32 v0, v0, v225
	v_lshlrev_b32_e32 v172, 16, v173
	v_and_b32_e32 v173, 0xffff0000, v173
	v_add_f32_e32 v0, v0, v172
	v_add_f32_e32 v0, v0, v173
	ds_bpermute_b32 v1, v204, v0
	s_waitcnt lgkmcnt(0)
	v_add_f32_e32 v0, v0, v1
	ds_bpermute_b32 v1, v205, v0
	s_waitcnt lgkmcnt(0)
	v_add_f32_e32 v0, v0, v1
	ds_bpermute_b32 v1, v206, v0
	s_waitcnt lgkmcnt(0)
	v_add_f32_e32 v0, v0, v1
	ds_bpermute_b32 v1, v207, v0
	s_waitcnt lgkmcnt(0)
	v_add_f32_e32 v0, v0, v1
	ds_bpermute_b32 v1, v208, v0
	s_waitcnt lgkmcnt(0)
	v_add_f32_e32 v161, v0, v1
	ds_bpermute_b32 v194, v209, v161
	ds_read_b128 v[0:3], v136
	ds_read_b128 v[4:7], v136 offset:8192
	s_waitcnt lgkmcnt(0)
	v_add_f32_e32 v161, v161, v194
	v_mul_f32_e32 v226, 0x3a000000, v161
	v_pk_add_f32 v[228:229], v[182:183], v[226:227] op_sel_hi:[1,0] neg_lo:[0,1] neg_hi:[0,1]
	v_pk_add_f32 v[232:233], v[174:175], v[226:227] op_sel_hi:[1,0] neg_lo:[0,1] neg_hi:[0,1]
	v_pk_mul_f32 v[230:231], v[228:229], v[228:229]
	v_pk_mul_f32 v[174:175], v[232:233], v[232:233]
	v_add_f32_e32 v161, v230, v231
	v_pk_add_f32 v[234:235], v[184:185], v[226:227] op_sel_hi:[1,0] neg_lo:[0,1] neg_hi:[0,1]
	v_add_f32_e32 v161, v174, v161
	v_pk_mul_f32 v[236:237], v[234:235], v[234:235]
	v_add_f32_e32 v161, v175, v161
	v_pk_add_f32 v[238:239], v[170:171], v[226:227] op_sel_hi:[1,0] neg_lo:[0,1] neg_hi:[0,1]
	v_add_f32_e32 v161, v236, v161
	v_pk_mul_f32 v[170:171], v[238:239], v[238:239]
	v_add_f32_e32 v161, v237, v161
	v_pk_add_f32 v[240:241], v[186:187], v[226:227] op_sel_hi:[1,0] neg_lo:[0,1] neg_hi:[0,1]
	v_add_f32_e32 v161, v170, v161
	v_pk_mul_f32 v[242:243], v[240:241], v[240:241]
	v_add_f32_e32 v161, v171, v161
	v_pk_add_f32 v[244:245], v[168:169], v[226:227] op_sel_hi:[1,0] neg_lo:[0,1] neg_hi:[0,1]
	v_add_f32_e32 v161, v242, v161
	v_pk_mul_f32 v[168:169], v[244:245], v[244:245]
	v_add_f32_e32 v161, v243, v161
	v_pk_add_f32 v[246:247], v[188:189], v[226:227] op_sel_hi:[1,0] neg_lo:[0,1] neg_hi:[0,1]
	v_add_f32_e32 v161, v168, v161
	v_pk_mul_f32 v[248:249], v[246:247], v[246:247]
	v_add_f32_e32 v161, v169, v161
	v_pk_add_f32 v[250:251], v[166:167], v[226:227] op_sel_hi:[1,0] neg_lo:[0,1] neg_hi:[0,1]
	v_add_f32_e32 v161, v248, v161
	v_pk_mul_f32 v[166:167], v[250:251], v[250:251]
	v_add_f32_e32 v161, v249, v161
	v_pk_add_f32 v[196:197], v[190:191], v[226:227] op_sel_hi:[1,0] neg_lo:[0,1] neg_hi:[0,1]
	v_add_f32_e32 v161, v166, v161
	v_pk_mul_f32 v[190:191], v[196:197], v[196:197]
	v_add_f32_e32 v161, v167, v161
	v_pk_add_f32 v[198:199], v[180:181], v[226:227] op_sel_hi:[1,0] neg_lo:[0,1] neg_hi:[0,1]
	v_add_f32_e32 v161, v190, v161
	v_pk_mul_f32 v[180:181], v[198:199], v[198:199]
	v_add_f32_e32 v161, v191, v161
	v_pk_add_f32 v[192:193], v[192:193], v[226:227] op_sel_hi:[1,0] neg_lo:[0,1] neg_hi:[0,1]
	v_add_f32_e32 v161, v180, v161
	v_pk_mul_f32 v[252:253], v[192:193], v[192:193]
	v_add_f32_e32 v161, v181, v161
	v_pk_add_f32 v[194:195], v[178:179], v[226:227] op_sel_hi:[1,0] neg_lo:[0,1] neg_hi:[0,1]
	v_add_f32_e32 v161, v252, v161
	v_pk_mul_f32 v[178:179], v[194:195], v[194:195]
	v_add_f32_e32 v161, v253, v161
	v_pk_add_f32 v[186:187], v[222:223], v[226:227] op_sel_hi:[1,0] neg_lo:[0,1] neg_hi:[0,1]
	v_add_f32_e32 v161, v178, v161
	v_pk_mul_f32 v[222:223], v[186:187], v[186:187]
	v_add_f32_e32 v161, v179, v161
	v_pk_add_f32 v[188:189], v[176:177], v[226:227] op_sel_hi:[1,0] neg_lo:[0,1] neg_hi:[0,1]
	v_add_f32_e32 v161, v222, v161
	v_pk_mul_f32 v[176:177], v[188:189], v[188:189]
	v_add_f32_e32 v161, v223, v161
	v_pk_add_f32 v[182:183], v[224:225], v[226:227] op_sel_hi:[1,0] neg_lo:[0,1] neg_hi:[0,1]
	v_add_f32_e32 v161, v176, v161
	v_pk_mul_f32 v[224:225], v[182:183], v[182:183]
	v_add_f32_e32 v161, v177, v161
	v_pk_add_f32 v[184:185], v[172:173], v[226:227] op_sel_hi:[1,0] neg_lo:[0,1] neg_hi:[0,1]
	v_add_f32_e32 v161, v224, v161
	v_pk_mul_f32 v[172:173], v[184:185], v[184:185]
	v_add_f32_e32 v161, v225, v161
	v_add_f32_e32 v161, v172, v161
	v_add_f32_e32 v161, v173, v161
	ds_bpermute_b32 v166, v204, v161
	v_add_u32_e32 v168, s33, v215
	v_add_u32_e32 v167, s33, v203
	v_cmp_gt_i32_e32 vcc, s26, v168
	s_waitcnt lgkmcnt(0)
; template <bool DRY = false>
; DI void phase_ln_router(const Params& p, char* smem, int bid, int nb) {
;     ...
;       {
;         const int tn2 = t + nb * 8;
;         const bf16_t* zr = p.z1b + (size_t)(tn2 < NTOK ? tn2 : t) * DM;
; #pragma unroll
;         for (int i = 0; i < 8; ++i) za[i] = *(const u32x2*)(zr + (i * 64 + lane) * 4);
;       }
;       float s = 0.f;
; #pragma unroll
;       for (int i = 0; i < 32; ++i) s += v[i];
;       s = wave_sum(s);
;       const float mu = s * (1.f / 2048.f);
;       float q = 0.f;
; #pragma unroll
;       for (int i = 0; i < 32; ++i) { const float d = v[i] - mu; q += d * d; }
;       q = wave_sum(q);
;       const float rs = rsqrtf(q * (1.f / 2048.f) + LN_EPS);
; #pragma unroll
;       for (int i = 0; i < 8; ++i) {
;         const int c = (i * 64 + lane) * 4;
;         const float4 gg = *(const float4*)(p.ln_mix_g + c);
;         const float4 bb = *(const float4*)(p.ln_mix_b + c);
;         float4 o;
;         o.x = (v[4 * i + 0] - mu) * rs * gg.x + bb.x;
;         o.y = (v[4 * i + 1] - mu) * rs * gg.y + bb.y;
;         o.z = (v[4 * i + 2] - mu) * rs * gg.z + bb.z;
;         o.w = (v[4 * i + 3] - mu) * rs * gg.w + bb.w;
;         { uint2 pk; pk.x = pack2(o.x, o.y); pk.y = pack2(o.z, o.w); *(uint2*)(p.h1b + (size_t)t * DM + c) = pk; }
;     ...
;         {
;           int pq = 0;
;           pq = __builtin_amdgcn_cvt_pk_fp8_f32(fminf(fmaxf(o.x * 16.f, -440.f), 440.f), fminf(fmaxf(o.y * 16.f, -440.f), 440.f), pq, false);
;           pq = __builtin_amdgcn_cvt_pk_fp8_f32(fminf(fmaxf(o.z * 16.f, -440.f), 440.f), fminf(fmaxf(o.w * 16.f, -440.f), 440.f), pq, true);
;           *(int*)(p.h1q + (size_t)t * DM + c) = pq;
;         }
	v_add_f32_e32 v161, v161, v166
	ds_bpermute_b32 v166, v205, v161
	s_waitcnt lgkmcnt(0)
	v_add_f32_e32 v161, v161, v166
	ds_bpermute_b32 v166, v206, v161
	s_waitcnt lgkmcnt(0)
	v_add_f32_e32 v161, v161, v166
	ds_bpermute_b32 v166, v207, v161
	s_waitcnt lgkmcnt(0)
	v_add_f32_e32 v161, v161, v166
	ds_bpermute_b32 v169, v208, v161
	v_cndmask_b32_e32 v166, v167, v168, vcc
	v_ashrrev_i32_e32 v167, 31, v166
	v_lshlrev_b64 v[166:167], 12, v[166:167]
	v_lshl_add_u64 v[172:173], v[158:159], 0, v[166:167]
	s_waitcnt lgkmcnt(0)
	v_add_f32_e32 v161, v161, v169
	ds_bpermute_b32 v176, v209, v161
	global_load_dwordx2 v[174:175], v[172:173], off
	global_load_dwordx2 v[170:171], v[172:173], off offset:512
	global_load_dwordx2 v[168:169], v[172:173], off offset:1024
	global_load_dwordx2 v[166:167], v[172:173], off offset:1536
	s_waitcnt lgkmcnt(0)
	v_add_f32_e32 v161, v161, v176
	v_fmamk_f32 v161, v161, 0x3a000000, v216
	v_mul_f32_e32 v176, 0x4b800000, v161
	v_cmp_gt_f32_e32 vcc, s1, v161
	s_nop 1
	v_cndmask_b32_e32 v161, v161, v176, vcc
	v_rsq_f32_e32 v161, v161
	global_load_dwordx2 v[180:181], v[172:173], off offset:2048
	global_load_dwordx2 v[178:179], v[172:173], off offset:2560
	global_load_dwordx2 v[176:177], v[172:173], off offset:3072
	s_nop 0
	global_load_dwordx2 v[172:173], v[172:173], off offset:3584
	v_mul_f32_e32 v190, 0x45800000, v161
	v_cndmask_b32_e32 v190, v161, v190, vcc
	v_pk_mul_f32 v[222:223], v[228:229], v[190:191] op_sel_hi:[1,0]
	v_pk_mul_f32 v[226:227], v[234:235], v[190:191] op_sel_hi:[1,0]
	s_waitcnt vmcnt(8)
	v_pk_fma_f32 v[0:1], v[0:1], v[222:223], v[4:5]
	v_pk_mul_f32 v[4:5], v[232:233], v[190:191] op_sel_hi:[1,0]
	v_pk_mul_f32 v[228:229], v[238:239], v[190:191] op_sel_hi:[1,0]
	v_pk_fma_f32 v[2:3], v[2:3], v[4:5], v[6:7]
	v_mul_f32_e32 v4, 0x41800000, v0
	v_mul_f32_e32 v5, 0x41800000, v1
	v_med3_f32 v4, v4, s29, v220
	v_med3_f32 v5, v5, s29, v220
	v_mov_b32_e32 v6, 0
	v_cvt_pk_fp8_f32 v6, v4, v5
	v_mul_f32_e32 v4, 0x41800000, v2
	v_mul_f32_e32 v5, 0x41800000, v3
	v_med3_f32 v4, v4, s29, v220
	v_med3_f32 v5, v5, s29, v220
	v_cvt_pk_fp8_f32 v6, v4, v5 op_sel:[0,0,1]
	v_cvt_pk_bf16_f32 v4, v0, v1
	v_cvt_pk_bf16_f32 v5, v2, v3
	global_store_dwordx2 v[164:165], v[4:5], off
	global_store_dword v[162:163], v6, off
	ds_read_b128 v[4:7], v136 offset:1024
	s_nop 0
	ds_read_b128 v[222:225], v136 offset:9216
	v_mov_b32_e32 v161, 0
	s_waitcnt lgkmcnt(0)
	v_pk_fma_f32 v[4:5], v[4:5], v[226:227], v[222:223]
	s_nop 0
	v_mul_f32_e32 v191, 0x41800000, v4
	v_mul_f32_e32 v222, 0x41800000, v5
	v_med3_f32 v191, v191, s29, v220
	v_med3_f32 v222, v222, s29, v220
	v_cvt_pk_fp8_f32 v161, v191, v222
	v_pk_fma_f32 v[6:7], v[6:7], v[228:229], v[224:225]
	s_nop 0
	v_mul_f32_e32 v223, 0x41800000, v6
	v_mul_f32_e32 v191, 0x41800000, v7
	v_med3_f32 v222, v223, s29, v220
	v_med3_f32 v191, v191, s29, v220
	v_cvt_pk_fp8_f32 v161, v222, v191 op_sel:[0,0,1]
	v_cvt_pk_bf16_f32 v222, v4, v5
	v_cvt_pk_bf16_f32 v223, v6, v7
	global_store_dwordx2 v[164:165], v[222:223], off offset:512
	global_store_dword v[162:163], v161, off offset:256
	ds_read_b128 v[222:225], v136 offset:2048
	s_nop 0
	ds_read_b128 v[226:229], v136 offset:10240
	v_pk_mul_f32 v[230:231], v[240:241], v[190:191] op_sel_hi:[1,0]
	v_pk_mul_f32 v[232:233], v[244:245], v[190:191] op_sel_hi:[1,0]
	v_mov_b32_e32 v161, 0
	s_waitcnt lgkmcnt(0)
	v_pk_fma_f32 v[222:223], v[222:223], v[230:231], v[226:227]
	s_nop 0
	v_mul_f32_e32 v191, 0x41800000, v222
	v_mul_f32_e32 v226, 0x41800000, v223
	v_med3_f32 v191, v191, s29, v220
	v_med3_f32 v226, v226, s29, v220
	v_cvt_pk_fp8_f32 v161, v191, v226
	v_pk_fma_f32 v[224:225], v[224:225], v[232:233], v[228:229]
	s_nop 0
	v_mul_f32_e32 v227, 0x41800000, v224
	v_mul_f32_e32 v191, 0x41800000, v225
	v_med3_f32 v226, v227, s29, v220
	v_med3_f32 v191, v191, s29, v220
	v_cvt_pk_fp8_f32 v161, v226, v191 op_sel:[0,0,1]
	v_cvt_pk_bf16_f32 v226, v222, v223
	v_cvt_pk_bf16_f32 v227, v224, v225
	global_store_dwordx2 v[164:165], v[226:227], off offset:1024
	global_store_dword v[162:163], v161, off offset:512
	ds_read_b128 v[226:229], v136 offset:3072
	s_nop 0
	ds_read_b128 v[230:233], v136 offset:11264
	v_pk_mul_f32 v[234:235], v[246:247], v[190:191] op_sel_hi:[1,0]
	v_pk_mul_f32 v[236:237], v[250:251], v[190:191] op_sel_hi:[1,0]
	v_mov_b32_e32 v161, 0
	s_waitcnt lgkmcnt(0)
	v_pk_fma_f32 v[226:227], v[226:227], v[234:235], v[230:231]
	s_nop 0
	v_mul_f32_e32 v191, 0x41800000, v226
	v_mul_f32_e32 v230, 0x41800000, v227
	v_med3_f32 v191, v191, s29, v220
	v_med3_f32 v230, v230, s29, v220
	v_cvt_pk_fp8_f32 v161, v191, v230
	v_pk_fma_f32 v[228:229], v[228:229], v[236:237], v[232:233]
	s_nop 0
	v_mul_f32_e32 v231, 0x41800000, v228
	v_mul_f32_e32 v191, 0x41800000, v229
	v_med3_f32 v230, v231, s29, v220
	v_med3_f32 v191, v191, s29, v220
	v_cvt_pk_fp8_f32 v161, v230, v191 op_sel:[0,0,1]
	v_cvt_pk_bf16_f32 v230, v226, v227
	v_cvt_pk_bf16_f32 v231, v228, v229
	global_store_dwordx2 v[164:165], v[230:231], off offset:1536
	global_store_dword v[162:163], v161, off offset:768
	ds_read_b128 v[230:233], v136 offset:4096
	s_nop 0
	ds_read_b128 v[234:237], v136 offset:12288
	v_pk_mul_f32 v[196:197], v[196:197], v[190:191] op_sel_hi:[1,0]
	v_pk_mul_f32 v[198:199], v[198:199], v[190:191] op_sel_hi:[1,0]
	v_mov_b32_e32 v161, 0
	s_waitcnt lgkmcnt(0)
; template <bool DRY = false>
; DI void phase_ln_router(const Params& p, char* smem, int bid, int nb) {
;     ...
; #pragma unroll
;       for (int i = 0; i < 8; ++i) {
;         const int c = (i * 64 + lane) * 4;
;         const float4 gg = *(const float4*)(p.ln_mix_g + c);
;         const float4 bb = *(const float4*)(p.ln_mix_b + c);
;         float4 o;
;         o.x = (v[4 * i + 0] - mu) * rs * gg.x + bb.x;
;         o.y = (v[4 * i + 1] - mu) * rs * gg.y + bb.y;
;         o.z = (v[4 * i + 2] - mu) * rs * gg.z + bb.z;
;         o.w = (v[4 * i + 3] - mu) * rs * gg.w + bb.w;
;         { uint2 pk; pk.x = pack2(o.x, o.y); pk.y = pack2(o.z, o.w); *(uint2*)(p.h1b + (size_t)t * DM + c) = pk; }
;     ...
;         {
;           int pq = 0;
;           pq = __builtin_amdgcn_cvt_pk_fp8_f32(fminf(fmaxf(o.x * 16.f, -440.f), 440.f), fminf(fmaxf(o.y * 16.f, -440.f), 440.f), pq, false);
;           pq = __builtin_amdgcn_cvt_pk_fp8_f32(fminf(fmaxf(o.z * 16.f, -440.f), 440.f), fminf(fmaxf(o.w * 16.f, -440.f), 440.f), pq, true);
;           *(int*)(p.h1q + (size_t)t * DM + c) = pq;
;         }
;     ...
;         *(float4*)(hs + wv * 2048 + c) = o;
;       }
;     }
;     __syncthreads();
;     {
;       f32x2_t acc[8];
; #pragma unroll
;       for (int j = 0; j < 8; ++j) acc[j] = (f32x2_t){0.f, 0.f};
; #pragma unroll
;       for (int j = 0; j < 8; ++j) {
; #pragma unroll
;         for (int i4 = 0; i4 < 16; ++i4) {
;           const float4 h = *(const float4*)(hs + j * 2048 + ks * 64 + 4 * i4);
;           acc[j] = __builtin_elementwise_fma((f32x2_t){h.x, h.x}, wr[4 * i4], acc[j]); acc[j] = __builtin_elementwise_fma((f32x2_t){h.y, h.y}, wr[4 * i4 + 1], acc[j]);
;           acc[j] = __builtin_elementwise_fma((f32x2_t){h.z, h.z}, wr[4 * i4 + 2], acc[j]); acc[j] = __builtin_elementwise_fma((f32x2_t){h.w, h.w}, wr[4 * i4 + 3], acc[j]);
	v_pk_fma_f32 v[196:197], v[196:197], v[230:231], v[234:235]
	s_nop 0
	v_mul_f32_e32 v191, 0x41800000, v196
	v_mul_f32_e32 v230, 0x41800000, v197
	v_med3_f32 v191, v191, s29, v220
	v_med3_f32 v230, v230, s29, v220
	v_cvt_pk_fp8_f32 v161, v191, v230
	v_pk_fma_f32 v[198:199], v[198:199], v[232:233], v[236:237]
	s_nop 0
	v_mul_f32_e32 v231, 0x41800000, v198
	v_mul_f32_e32 v191, 0x41800000, v199
	v_med3_f32 v230, v231, s29, v220
	v_med3_f32 v191, v191, s29, v220
	v_cvt_pk_fp8_f32 v161, v230, v191 op_sel:[0,0,1]
	v_cvt_pk_bf16_f32 v230, v196, v197
	v_cvt_pk_bf16_f32 v231, v198, v199
	global_store_dwordx2 v[164:165], v[230:231], off offset:2048
	global_store_dword v[162:163], v161, off offset:1024
	ds_read_b128 v[230:233], v136 offset:5120
	s_nop 0
	ds_read_b128 v[234:237], v136 offset:13312
	v_pk_mul_f32 v[192:193], v[192:193], v[190:191] op_sel_hi:[1,0]
	v_pk_mul_f32 v[194:195], v[194:195], v[190:191] op_sel_hi:[1,0]
	v_mov_b32_e32 v161, 0
	s_waitcnt lgkmcnt(0)
	v_pk_fma_f32 v[192:193], v[192:193], v[230:231], v[234:235]
	s_nop 0
	v_mul_f32_e32 v191, 0x41800000, v192
	v_mul_f32_e32 v230, 0x41800000, v193
	v_med3_f32 v191, v191, s29, v220
	v_med3_f32 v230, v230, s29, v220
	v_cvt_pk_fp8_f32 v161, v191, v230
	v_pk_fma_f32 v[194:195], v[194:195], v[232:233], v[236:237]
	s_nop 0
	v_mul_f32_e32 v231, 0x41800000, v194
	v_mul_f32_e32 v191, 0x41800000, v195
	v_med3_f32 v230, v231, s29, v220
	v_med3_f32 v191, v191, s29, v220
	v_cvt_pk_fp8_f32 v161, v230, v191 op_sel:[0,0,1]
	v_cvt_pk_bf16_f32 v230, v192, v193
	v_cvt_pk_bf16_f32 v231, v194, v195
	global_store_dwordx2 v[164:165], v[230:231], off offset:2560
	global_store_dword v[162:163], v161, off offset:1280
	ds_read_b128 v[230:233], v136 offset:6144
	s_nop 0
	ds_read_b128 v[234:237], v136 offset:14336
	v_pk_mul_f32 v[186:187], v[186:187], v[190:191] op_sel_hi:[1,0]
	v_pk_mul_f32 v[188:189], v[188:189], v[190:191] op_sel_hi:[1,0]
	v_mov_b32_e32 v161, 0
	s_waitcnt lgkmcnt(0)
	v_pk_fma_f32 v[186:187], v[186:187], v[230:231], v[234:235]
	s_nop 0
	v_mul_f32_e32 v191, 0x41800000, v186
	v_mul_f32_e32 v230, 0x41800000, v187
	v_med3_f32 v191, v191, s29, v220
	v_med3_f32 v230, v230, s29, v220
	v_cvt_pk_fp8_f32 v161, v191, v230
	v_pk_fma_f32 v[188:189], v[188:189], v[232:233], v[236:237]
	s_nop 0
	v_mul_f32_e32 v231, 0x41800000, v188
	v_mul_f32_e32 v191, 0x41800000, v189
	v_med3_f32 v230, v231, s29, v220
	v_med3_f32 v191, v191, s29, v220
	v_cvt_pk_fp8_f32 v161, v230, v191 op_sel:[0,0,1]
	v_cvt_pk_bf16_f32 v230, v186, v187
	v_cvt_pk_bf16_f32 v231, v188, v189
	global_store_dwordx2 v[164:165], v[230:231], off offset:3072
	global_store_dword v[162:163], v161, off offset:1536
	ds_read_b128 v[230:233], v136 offset:7168
	s_nop 0
	ds_read_b128 v[234:237], v136 offset:15360
	v_pk_mul_f32 v[182:183], v[182:183], v[190:191] op_sel_hi:[1,0]
	ds_write_b128 v213, v[0:3] offset:16
	ds_write_b128 v213, v[4:7] offset:1040
	ds_write_b128 v213, v[222:225] offset:2064
	ds_write_b128 v213, v[226:229] offset:3088
	ds_write_b128 v213, v[196:199] offset:4112
	ds_write_b128 v213, v[192:195] offset:5136
	ds_write_b128 v213, v[186:189] offset:6160
	v_mov_b32_e32 v161, 0
	v_pk_mul_f32 v[184:185], v[184:185], v[190:191] op_sel_hi:[1,0]
	s_waitcnt lgkmcnt(0)
	v_pk_fma_f32 v[0:1], v[182:183], v[230:231], v[234:235]
	s_nop 0
	v_mul_f32_e32 v5, 0x41800000, v0
	v_mul_f32_e32 v6, 0x41800000, v1
	v_med3_f32 v5, v5, s29, v220
	v_med3_f32 v6, v6, s29, v220
	v_cvt_pk_fp8_f32 v161, v5, v6
	v_pk_fma_f32 v[2:3], v[184:185], v[232:233], v[236:237]
	v_cvt_pk_bf16_f32 v4, v0, v1
	v_mul_f32_e32 v7, 0x41800000, v2
	v_mul_f32_e32 v5, 0x41800000, v3
	v_med3_f32 v6, v7, s29, v220
	v_med3_f32 v5, v5, s29, v220
	v_cvt_pk_fp8_f32 v161, v6, v5 op_sel:[0,0,1]
	v_cvt_pk_bf16_f32 v5, v2, v3
	ds_write_b128 v213, v[0:3] offset:7184
	global_store_dwordx2 v[164:165], v[4:5], off offset:3584
	global_store_dword v[162:163], v161, off offset:1792
	s_waitcnt lgkmcnt(0)
	s_barrier
	ds_read_b128 v[0:3], v210 offset:16
	ds_read_b128 v[4:7], v210 offset:32
	ds_read_b128 v[182:185], v210 offset:48
	ds_read_b128 v[186:189], v210 offset:64
	ds_read_b128 v[192:195], v210 offset:80
	ds_read_b128 v[196:199], v210 offset:96
	ds_read_b128 v[222:225], v210 offset:112
	ds_read_b128 v[226:229], v210 offset:128
	s_waitcnt lgkmcnt(7)
	v_pk_fma_f32 v[190:191], v[0:1], v[8:9], 0 op_sel_hi:[0,1,0]
	v_pk_fma_f32 v[0:1], v[0:1], v[10:11], v[190:191] op_sel:[1,0,0]
	v_mov_b32_e32 v230, v3
	v_pk_fma_f32 v[0:1], v[2:3], v[12:13], v[0:1] op_sel_hi:[0,1,1]
	v_pk_fma_f32 v[0:1], v[230:231], v[14:15], v[0:1] op_sel_hi:[0,1,1]
	s_waitcnt lgkmcnt(6)
	v_pk_fma_f32 v[0:1], v[4:5], v[16:17], v[0:1] op_sel_hi:[0,1,1]
	v_pk_fma_f32 v[0:1], v[4:5], v[18:19], v[0:1] op_sel:[1,0,0]
	v_mov_b32_e32 v232, v7
	v_pk_fma_f32 v[0:1], v[6:7], v[20:21], v[0:1] op_sel_hi:[0,1,1]
	v_pk_fma_f32 v[0:1], v[232:233], v[22:23], v[0:1] op_sel_hi:[0,1,1]
	s_waitcnt lgkmcnt(5)
	v_pk_fma_f32 v[0:1], v[182:183], v[24:25], v[0:1] op_sel_hi:[0,1,1]
	v_pk_fma_f32 v[0:1], v[182:183], v[26:27], v[0:1] op_sel:[1,0,0]
	v_mov_b32_e32 v234, v185
	v_pk_fma_f32 v[0:1], v[184:185], v[28:29], v[0:1] op_sel_hi:[0,1,1]
	v_pk_fma_f32 v[0:1], v[234:235], v[30:31], v[0:1] op_sel_hi:[0,1,1]
	s_waitcnt lgkmcnt(4)
	v_pk_fma_f32 v[0:1], v[186:187], v[32:33], v[0:1] op_sel_hi:[0,1,1]
	v_pk_fma_f32 v[0:1], v[186:187], v[34:35], v[0:1] op_sel:[1,0,0]
	v_mov_b32_e32 v236, v189
	v_pk_fma_f32 v[0:1], v[188:189], v[36:37], v[0:1] op_sel_hi:[0,1,1]
	v_pk_fma_f32 v[0:1], v[236:237], v[38:39], v[0:1] op_sel_hi:[0,1,1]
	s_waitcnt lgkmcnt(3)
; template <bool DRY = false>
; DI void phase_ln_router(const Params& p, char* smem, int bid, int nb) {
;     ...
;       f32x2_t acc[8];
; #pragma unroll
;       for (int j = 0; j < 8; ++j) acc[j] = (f32x2_t){0.f, 0.f};
; #pragma unroll
;       for (int j = 0; j < 8; ++j) {
; #pragma unroll
;         for (int i4 = 0; i4 < 16; ++i4) {
;           const float4 h = *(const float4*)(hs + j * 2048 + ks * 64 + 4 * i4);
;           acc[j] = __builtin_elementwise_fma((f32x2_t){h.x, h.x}, wr[4 * i4], acc[j]); acc[j] = __builtin_elementwise_fma((f32x2_t){h.y, h.y}, wr[4 * i4 + 1], acc[j]);
;           acc[j] = __builtin_elementwise_fma((f32x2_t){h.z, h.z}, wr[4 * i4 + 2], acc[j]); acc[j] = __builtin_elementwise_fma((f32x2_t){h.w, h.w}, wr[4 * i4 + 3], acc[j]);
;           if ((i4 & 7) == 7) __builtin_amdgcn_sched_barrier(0);
;         }
;       }
	v_pk_fma_f32 v[0:1], v[192:193], v[40:41], v[0:1] op_sel_hi:[0,1,1]
	v_pk_fma_f32 v[0:1], v[192:193], v[42:43], v[0:1] op_sel:[1,0,0]
	v_mov_b32_e32 v238, v195
	v_pk_fma_f32 v[0:1], v[194:195], v[44:45], v[0:1] op_sel_hi:[0,1,1]
	v_pk_fma_f32 v[0:1], v[238:239], v[46:47], v[0:1] op_sel_hi:[0,1,1]
	s_waitcnt lgkmcnt(2)
	v_pk_fma_f32 v[0:1], v[196:197], v[48:49], v[0:1] op_sel_hi:[0,1,1]
	v_pk_fma_f32 v[0:1], v[196:197], v[50:51], v[0:1] op_sel:[1,0,0]
	v_mov_b32_e32 v240, v199
	v_pk_fma_f32 v[0:1], v[198:199], v[52:53], v[0:1] op_sel_hi:[0,1,1]
	v_pk_fma_f32 v[0:1], v[240:241], v[54:55], v[0:1] op_sel_hi:[0,1,1]
	s_waitcnt lgkmcnt(1)
	v_pk_fma_f32 v[0:1], v[222:223], v[56:57], v[0:1] op_sel_hi:[0,1,1]
	v_pk_fma_f32 v[0:1], v[222:223], v[58:59], v[0:1] op_sel:[1,0,0]
	v_mov_b32_e32 v242, v225
	v_pk_fma_f32 v[0:1], v[224:225], v[60:61], v[0:1] op_sel_hi:[0,1,1]
	v_pk_fma_f32 v[0:1], v[242:243], v[62:63], v[0:1] op_sel_hi:[0,1,1]
	s_waitcnt lgkmcnt(0)
	v_pk_fma_f32 v[0:1], v[226:227], v[64:65], v[0:1] op_sel_hi:[0,1,1]
	v_pk_fma_f32 v[0:1], v[226:227], v[66:67], v[0:1] op_sel:[1,0,0]
	v_mov_b32_e32 v2, v229
	v_pk_fma_f32 v[0:1], v[228:229], v[68:69], v[0:1] op_sel_hi:[0,1,1]
	v_pk_fma_f32 v[190:191], v[2:3], v[70:71], v[0:1] op_sel_hi:[0,1,1]
	ds_read_b128 v[0:3], v210 offset:144
	ds_read_b128 v[4:7], v210 offset:160
	ds_read_b128 v[182:185], v210 offset:176
	ds_read_b128 v[186:189], v210 offset:192
	s_waitcnt lgkmcnt(3)
	v_pk_fma_f32 v[190:191], v[0:1], v[72:73], v[190:191] op_sel_hi:[0,1,1]
	v_pk_fma_f32 v[0:1], v[0:1], v[74:75], v[190:191] op_sel:[1,0,0]
	v_mov_b32_e32 v192, v3
	v_pk_fma_f32 v[0:1], v[2:3], v[76:77], v[0:1] op_sel_hi:[0,1,1]
	v_pk_fma_f32 v[0:1], v[192:193], v[78:79], v[0:1] op_sel_hi:[0,1,1]
	s_waitcnt lgkmcnt(2)
	v_pk_fma_f32 v[0:1], v[4:5], v[80:81], v[0:1] op_sel_hi:[0,1,1]
	v_pk_fma_f32 v[0:1], v[4:5], v[82:83], v[0:1] op_sel:[1,0,0]
	v_mov_b32_e32 v2, v7
	v_pk_fma_f32 v[0:1], v[6:7], v[84:85], v[0:1] op_sel_hi:[0,1,1]
	v_pk_fma_f32 v[0:1], v[2:3], v[86:87], v[0:1] op_sel_hi:[0,1,1]
	s_waitcnt lgkmcnt(1)
	v_pk_fma_f32 v[0:1], v[182:183], v[88:89], v[0:1] op_sel_hi:[0,1,1]
	v_pk_fma_f32 v[0:1], v[182:183], v[90:91], v[0:1] op_sel:[1,0,0]
	v_mov_b32_e32 v2, v185
	v_pk_fma_f32 v[0:1], v[184:185], v[92:93], v[0:1] op_sel_hi:[0,1,1]
	v_pk_fma_f32 v[0:1], v[2:3], v[94:95], v[0:1] op_sel_hi:[0,1,1]
	s_waitcnt lgkmcnt(0)
	v_pk_fma_f32 v[0:1], v[186:187], v[96:97], v[0:1] op_sel_hi:[0,1,1]
	v_pk_fma_f32 v[4:5], v[186:187], v[98:99], v[0:1] op_sel:[1,0,0]
	ds_read_b128 v[0:3], v210 offset:208
	v_pk_fma_f32 v[4:5], v[188:189], v[100:101], v[4:5] op_sel_hi:[0,1,1]
	v_mov_b32_e32 v6, v189
	v_pk_fma_f32 v[182:183], v[6:7], v[102:103], v[4:5] op_sel_hi:[0,1,1]
	ds_read_b128 v[4:7], v210 offset:224
	s_waitcnt lgkmcnt(1)
	v_pk_fma_f32 v[182:183], v[0:1], v[104:105], v[182:183] op_sel_hi:[0,1,1]
	v_pk_fma_f32 v[0:1], v[0:1], v[106:107], v[182:183] op_sel:[1,0,0]
	s_nop 0
	v_pk_fma_f32 v[0:1], v[2:3], v[108:109], v[0:1] op_sel_hi:[0,1,1]
	v_mov_b32_e32 v2, v3
	v_pk_fma_f32 v[0:1], v[2:3], v[110:111], v[0:1] op_sel_hi:[0,1,1]
	s_waitcnt lgkmcnt(0)
	v_pk_fma_f32 v[0:1], v[4:5], v[112:113], v[0:1] op_sel_hi:[0,1,1]
	v_pk_fma_f32 v[4:5], v[4:5], v[114:115], v[0:1] op_sel:[1,0,0]
	ds_read_b128 v[0:3], v210 offset:240
	v_pk_fma_f32 v[4:5], v[6:7], v[116:117], v[4:5] op_sel_hi:[0,1,1]
	v_mov_b32_e32 v6, v7
	v_pk_fma_f32 v[182:183], v[6:7], v[118:119], v[4:5] op_sel_hi:[0,1,1]
	ds_read_b128 v[4:7], v210 offset:256
	s_waitcnt lgkmcnt(1)
	v_pk_fma_f32 v[182:183], v[0:1], v[120:121], v[182:183] op_sel_hi:[0,1,1]
	v_pk_fma_f32 v[0:1], v[0:1], v[122:123], v[182:183] op_sel:[1,0,0]
	s_nop 0
	v_pk_fma_f32 v[0:1], v[2:3], v[124:125], v[0:1] op_sel_hi:[0,1,1]
	v_mov_b32_e32 v2, v3
	v_pk_fma_f32 v[0:1], v[2:3], v[126:127], v[0:1] op_sel_hi:[0,1,1]
	s_waitcnt lgkmcnt(0)
	v_pk_fma_f32 v[0:1], v[4:5], v[128:129], v[0:1] op_sel_hi:[0,1,1]
	v_pk_fma_f32 v[0:1], v[4:5], v[130:131], v[0:1] op_sel:[1,0,0]
	v_mov_b32_e32 v2, v7
	v_pk_fma_f32 v[0:1], v[6:7], v[132:133], v[0:1] op_sel_hi:[0,1,1]
	v_pk_fma_f32 v[0:1], v[2:3], v[134:135], v[0:1] op_sel_hi:[0,1,1]
	ds_read_b128 v[2:5], v210 offset:8208
	ds_read_b128 v[182:185], v210 offset:8224
	ds_read_b128 v[186:189], v210 offset:8240
	ds_read_b128 v[192:195], v210 offset:8256
	s_waitcnt lgkmcnt(3)
	v_pk_fma_f32 v[6:7], v[2:3], v[8:9], 0 op_sel_hi:[0,1,0]
	v_pk_fma_f32 v[2:3], v[2:3], v[10:11], v[6:7] op_sel:[1,0,0]
	v_mov_b32_e32 v190, v5
	v_pk_fma_f32 v[2:3], v[4:5], v[12:13], v[2:3] op_sel_hi:[0,1,1]
	v_pk_fma_f32 v[2:3], v[190:191], v[14:15], v[2:3] op_sel_hi:[0,1,1]
	s_waitcnt lgkmcnt(2)
	v_pk_fma_f32 v[2:3], v[182:183], v[16:17], v[2:3] op_sel_hi:[0,1,1]
	v_pk_fma_f32 v[2:3], v[182:183], v[18:19], v[2:3] op_sel:[1,0,0]
	v_mov_b32_e32 v4, v185
	v_pk_fma_f32 v[2:3], v[184:185], v[20:21], v[2:3] op_sel_hi:[0,1,1]
	v_pk_fma_f32 v[2:3], v[4:5], v[22:23], v[2:3] op_sel_hi:[0,1,1]
	s_waitcnt lgkmcnt(1)
	v_pk_fma_f32 v[2:3], v[186:187], v[24:25], v[2:3] op_sel_hi:[0,1,1]
	v_pk_fma_f32 v[2:3], v[186:187], v[26:27], v[2:3] op_sel:[1,0,0]
	v_mov_b32_e32 v4, v189
	v_pk_fma_f32 v[2:3], v[188:189], v[28:29], v[2:3] op_sel_hi:[0,1,1]
	v_pk_fma_f32 v[2:3], v[4:5], v[30:31], v[2:3] op_sel_hi:[0,1,1]
	s_waitcnt lgkmcnt(0)
	v_pk_fma_f32 v[2:3], v[192:193], v[32:33], v[2:3] op_sel_hi:[0,1,1]
	v_pk_fma_f32 v[6:7], v[192:193], v[34:35], v[2:3] op_sel:[1,0,0]
	ds_read_b128 v[2:5], v210 offset:8272
	v_pk_fma_f32 v[6:7], v[194:195], v[36:37], v[6:7] op_sel_hi:[0,1,1]
	v_mov_b32_e32 v182, v195
	v_pk_fma_f32 v[6:7], v[182:183], v[38:39], v[6:7] op_sel_hi:[0,1,1]
	ds_read_b128 v[182:185], v210 offset:8288
	s_waitcnt lgkmcnt(1)
; template <bool DRY = false>
; DI void phase_ln_router(const Params& p, char* smem, int bid, int nb) {
;     ...
;       f32x2_t acc[8];
; #pragma unroll
;       for (int j = 0; j < 8; ++j) acc[j] = (f32x2_t){0.f, 0.f};
; #pragma unroll
;       for (int j = 0; j < 8; ++j) {
; #pragma unroll
;         for (int i4 = 0; i4 < 16; ++i4) {
;           const float4 h = *(const float4*)(hs + j * 2048 + ks * 64 + 4 * i4);
;           acc[j] = __builtin_elementwise_fma((f32x2_t){h.x, h.x}, wr[4 * i4], acc[j]); acc[j] = __builtin_elementwise_fma((f32x2_t){h.y, h.y}, wr[4 * i4 + 1], acc[j]);
;           acc[j] = __builtin_elementwise_fma((f32x2_t){h.z, h.z}, wr[4 * i4 + 2], acc[j]); acc[j] = __builtin_elementwise_fma((f32x2_t){h.w, h.w}, wr[4 * i4 + 3], acc[j]);
;           if ((i4 & 7) == 7) __builtin_amdgcn_sched_barrier(0);
;         }
;       }
	v_pk_fma_f32 v[6:7], v[2:3], v[40:41], v[6:7] op_sel_hi:[0,1,1]
	v_pk_fma_f32 v[2:3], v[2:3], v[42:43], v[6:7] op_sel:[1,0,0]
	s_nop 0
	v_pk_fma_f32 v[2:3], v[4:5], v[44:45], v[2:3] op_sel_hi:[0,1,1]
	v_mov_b32_e32 v4, v5
	v_pk_fma_f32 v[2:3], v[4:5], v[46:47], v[2:3] op_sel_hi:[0,1,1]
	s_waitcnt lgkmcnt(0)
	v_pk_fma_f32 v[2:3], v[182:183], v[48:49], v[2:3] op_sel_hi:[0,1,1]
	v_pk_fma_f32 v[6:7], v[182:183], v[50:51], v[2:3] op_sel:[1,0,0]
	ds_read_b128 v[2:5], v210 offset:8304
	v_pk_fma_f32 v[6:7], v[184:185], v[52:53], v[6:7] op_sel_hi:[0,1,1]
	v_mov_b32_e32 v182, v185
	v_pk_fma_f32 v[6:7], v[182:183], v[54:55], v[6:7] op_sel_hi:[0,1,1]
	ds_read_b128 v[182:185], v210 offset:8320
	s_waitcnt lgkmcnt(1)
	v_pk_fma_f32 v[6:7], v[2:3], v[56:57], v[6:7] op_sel_hi:[0,1,1]
	v_pk_fma_f32 v[2:3], v[2:3], v[58:59], v[6:7] op_sel:[1,0,0]
	s_nop 0
	v_pk_fma_f32 v[2:3], v[4:5], v[60:61], v[2:3] op_sel_hi:[0,1,1]
	v_mov_b32_e32 v4, v5
	v_pk_fma_f32 v[2:3], v[4:5], v[62:63], v[2:3] op_sel_hi:[0,1,1]
	s_waitcnt lgkmcnt(0)
	v_pk_fma_f32 v[2:3], v[182:183], v[64:65], v[2:3] op_sel_hi:[0,1,1]
	v_pk_fma_f32 v[2:3], v[182:183], v[66:67], v[2:3] op_sel:[1,0,0]
	v_mov_b32_e32 v4, v185
	v_pk_fma_f32 v[2:3], v[184:185], v[68:69], v[2:3] op_sel_hi:[0,1,1]
	v_pk_fma_f32 v[6:7], v[4:5], v[70:71], v[2:3] op_sel_hi:[0,1,1]
	ds_read_b128 v[2:5], v210 offset:8336
	ds_read_b128 v[182:185], v210 offset:8352
	ds_read_b128 v[186:189], v210 offset:8368
	ds_read_b128 v[192:195], v210 offset:8384
	s_waitcnt lgkmcnt(3)
	v_pk_fma_f32 v[6:7], v[2:3], v[72:73], v[6:7] op_sel_hi:[0,1,1]
	v_pk_fma_f32 v[2:3], v[2:3], v[74:75], v[6:7] op_sel:[1,0,0]
	v_mov_b32_e32 v190, v5
	v_pk_fma_f32 v[2:3], v[4:5], v[76:77], v[2:3] op_sel_hi:[0,1,1]
	v_pk_fma_f32 v[2:3], v[190:191], v[78:79], v[2:3] op_sel_hi:[0,1,1]
	s_waitcnt lgkmcnt(2)
	v_pk_fma_f32 v[2:3], v[182:183], v[80:81], v[2:3] op_sel_hi:[0,1,1]
	v_pk_fma_f32 v[2:3], v[182:183], v[82:83], v[2:3] op_sel:[1,0,0]
	v_mov_b32_e32 v4, v185
	v_pk_fma_f32 v[2:3], v[184:185], v[84:85], v[2:3] op_sel_hi:[0,1,1]
	v_pk_fma_f32 v[2:3], v[4:5], v[86:87], v[2:3] op_sel_hi:[0,1,1]
	s_waitcnt lgkmcnt(1)
	v_pk_fma_f32 v[2:3], v[186:187], v[88:89], v[2:3] op_sel_hi:[0,1,1]
	v_pk_fma_f32 v[2:3], v[186:187], v[90:91], v[2:3] op_sel:[1,0,0]
	v_mov_b32_e32 v4, v189
	v_pk_fma_f32 v[2:3], v[188:189], v[92:93], v[2:3] op_sel_hi:[0,1,1]
	v_pk_fma_f32 v[2:3], v[4:5], v[94:95], v[2:3] op_sel_hi:[0,1,1]
	s_waitcnt lgkmcnt(0)
	v_pk_fma_f32 v[2:3], v[192:193], v[96:97], v[2:3] op_sel_hi:[0,1,1]
	v_pk_fma_f32 v[6:7], v[192:193], v[98:99], v[2:3] op_sel:[1,0,0]
	ds_read_b128 v[2:5], v210 offset:8400
	v_pk_fma_f32 v[6:7], v[194:195], v[100:101], v[6:7] op_sel_hi:[0,1,1]
	v_mov_b32_e32 v182, v195
	v_pk_fma_f32 v[6:7], v[182:183], v[102:103], v[6:7] op_sel_hi:[0,1,1]
	ds_read_b128 v[182:185], v210 offset:8416
	s_waitcnt lgkmcnt(1)
	v_pk_fma_f32 v[6:7], v[2:3], v[104:105], v[6:7] op_sel_hi:[0,1,1]
	v_pk_fma_f32 v[2:3], v[2:3], v[106:107], v[6:7] op_sel:[1,0,0]
	s_nop 0
	v_pk_fma_f32 v[2:3], v[4:5], v[108:109], v[2:3] op_sel_hi:[0,1,1]
	v_mov_b32_e32 v4, v5
	v_pk_fma_f32 v[2:3], v[4:5], v[110:111], v[2:3] op_sel_hi:[0,1,1]
	s_waitcnt lgkmcnt(0)
	v_pk_fma_f32 v[2:3], v[182:183], v[112:113], v[2:3] op_sel_hi:[0,1,1]
	v_pk_fma_f32 v[6:7], v[182:183], v[114:115], v[2:3] op_sel:[1,0,0]
	ds_read_b128 v[2:5], v210 offset:8432
	v_pk_fma_f32 v[6:7], v[184:185], v[116:117], v[6:7] op_sel_hi:[0,1,1]
	v_mov_b32_e32 v182, v185
	v_pk_fma_f32 v[6:7], v[182:183], v[118:119], v[6:7] op_sel_hi:[0,1,1]
	ds_read_b128 v[182:185], v210 offset:8448
	s_waitcnt lgkmcnt(1)
	v_pk_fma_f32 v[6:7], v[2:3], v[120:121], v[6:7] op_sel_hi:[0,1,1]
	v_pk_fma_f32 v[2:3], v[2:3], v[122:123], v[6:7] op_sel:[1,0,0]
	s_nop 0
	v_pk_fma_f32 v[2:3], v[4:5], v[124:125], v[2:3] op_sel_hi:[0,1,1]
	v_mov_b32_e32 v4, v5
	v_pk_fma_f32 v[2:3], v[4:5], v[126:127], v[2:3] op_sel_hi:[0,1,1]
	s_waitcnt lgkmcnt(0)
	v_pk_fma_f32 v[2:3], v[182:183], v[128:129], v[2:3] op_sel_hi:[0,1,1]
	v_pk_fma_f32 v[2:3], v[182:183], v[130:131], v[2:3] op_sel:[1,0,0]
	v_mov_b32_e32 v4, v185
	v_pk_fma_f32 v[2:3], v[184:185], v[132:133], v[2:3] op_sel_hi:[0,1,1]
	v_pk_fma_f32 v[2:3], v[4:5], v[134:135], v[2:3] op_sel_hi:[0,1,1]
	ds_read_b128 v[4:7], v210 offset:16400
	ds_read_b128 v[182:185], v210 offset:16416
	ds_read_b128 v[186:189], v210 offset:16432
	ds_read_b128 v[192:195], v210 offset:16448
	s_waitcnt lgkmcnt(3)
	v_pk_fma_f32 v[190:191], v[4:5], v[8:9], 0 op_sel_hi:[0,1,0]
	v_pk_fma_f32 v[4:5], v[4:5], v[10:11], v[190:191] op_sel:[1,0,0]
	v_mov_b32_e32 v196, v7
	v_pk_fma_f32 v[4:5], v[6:7], v[12:13], v[4:5] op_sel_hi:[0,1,1]
	v_pk_fma_f32 v[4:5], v[196:197], v[14:15], v[4:5] op_sel_hi:[0,1,1]
	s_waitcnt lgkmcnt(2)
	v_pk_fma_f32 v[4:5], v[182:183], v[16:17], v[4:5] op_sel_hi:[0,1,1]
	v_pk_fma_f32 v[4:5], v[182:183], v[18:19], v[4:5] op_sel:[1,0,0]
	v_mov_b32_e32 v6, v185
	v_pk_fma_f32 v[4:5], v[184:185], v[20:21], v[4:5] op_sel_hi:[0,1,1]
	v_pk_fma_f32 v[4:5], v[6:7], v[22:23], v[4:5] op_sel_hi:[0,1,1]
	s_waitcnt lgkmcnt(1)
	v_pk_fma_f32 v[4:5], v[186:187], v[24:25], v[4:5] op_sel_hi:[0,1,1]
	v_pk_fma_f32 v[4:5], v[186:187], v[26:27], v[4:5] op_sel:[1,0,0]
	v_mov_b32_e32 v6, v189
	v_pk_fma_f32 v[4:5], v[188:189], v[28:29], v[4:5] op_sel_hi:[0,1,1]
	v_pk_fma_f32 v[4:5], v[6:7], v[30:31], v[4:5] op_sel_hi:[0,1,1]
	s_waitcnt lgkmcnt(0)
	v_pk_fma_f32 v[4:5], v[192:193], v[32:33], v[4:5] op_sel_hi:[0,1,1]
	v_pk_fma_f32 v[182:183], v[192:193], v[34:35], v[4:5] op_sel:[1,0,0]
	ds_read_b128 v[4:7], v210 offset:16464
	v_pk_fma_f32 v[182:183], v[194:195], v[36:37], v[182:183] op_sel_hi:[0,1,1]
	v_mov_b32_e32 v184, v195
	v_pk_fma_f32 v[186:187], v[184:185], v[38:39], v[182:183] op_sel_hi:[0,1,1]
	ds_read_b128 v[182:185], v210 offset:16480
	s_waitcnt lgkmcnt(1)
; template <bool DRY = false>
; DI void phase_ln_router(const Params& p, char* smem, int bid, int nb) {
;     ...
;       f32x2_t acc[8];
; #pragma unroll
;       for (int j = 0; j < 8; ++j) acc[j] = (f32x2_t){0.f, 0.f};
; #pragma unroll
;       for (int j = 0; j < 8; ++j) {
; #pragma unroll
;         for (int i4 = 0; i4 < 16; ++i4) {
;           const float4 h = *(const float4*)(hs + j * 2048 + ks * 64 + 4 * i4);
;           acc[j] = __builtin_elementwise_fma((f32x2_t){h.x, h.x}, wr[4 * i4], acc[j]); acc[j] = __builtin_elementwise_fma((f32x2_t){h.y, h.y}, wr[4 * i4 + 1], acc[j]);
;           acc[j] = __builtin_elementwise_fma((f32x2_t){h.z, h.z}, wr[4 * i4 + 2], acc[j]); acc[j] = __builtin_elementwise_fma((f32x2_t){h.w, h.w}, wr[4 * i4 + 3], acc[j]);
;           if ((i4 & 7) == 7) __builtin_amdgcn_sched_barrier(0);
;         }
;       }
	v_pk_fma_f32 v[186:187], v[4:5], v[40:41], v[186:187] op_sel_hi:[0,1,1]
	v_pk_fma_f32 v[4:5], v[4:5], v[42:43], v[186:187] op_sel:[1,0,0]
	s_nop 0
	v_pk_fma_f32 v[4:5], v[6:7], v[44:45], v[4:5] op_sel_hi:[0,1,1]
	v_mov_b32_e32 v6, v7
	v_pk_fma_f32 v[4:5], v[6:7], v[46:47], v[4:5] op_sel_hi:[0,1,1]
	s_waitcnt lgkmcnt(0)
	v_pk_fma_f32 v[4:5], v[182:183], v[48:49], v[4:5] op_sel_hi:[0,1,1]
	v_pk_fma_f32 v[182:183], v[182:183], v[50:51], v[4:5] op_sel:[1,0,0]
	ds_read_b128 v[4:7], v210 offset:16496
	v_pk_fma_f32 v[182:183], v[184:185], v[52:53], v[182:183] op_sel_hi:[0,1,1]
	v_mov_b32_e32 v184, v185
	v_pk_fma_f32 v[186:187], v[184:185], v[54:55], v[182:183] op_sel_hi:[0,1,1]
	ds_read_b128 v[182:185], v210 offset:16512
	s_waitcnt lgkmcnt(1)
	v_pk_fma_f32 v[186:187], v[4:5], v[56:57], v[186:187] op_sel_hi:[0,1,1]
	v_pk_fma_f32 v[4:5], v[4:5], v[58:59], v[186:187] op_sel:[1,0,0]
	s_nop 0
	v_pk_fma_f32 v[4:5], v[6:7], v[60:61], v[4:5] op_sel_hi:[0,1,1]
	v_mov_b32_e32 v6, v7
	v_pk_fma_f32 v[4:5], v[6:7], v[62:63], v[4:5] op_sel_hi:[0,1,1]
	s_waitcnt lgkmcnt(0)
	v_pk_fma_f32 v[4:5], v[182:183], v[64:65], v[4:5] op_sel_hi:[0,1,1]
	v_pk_fma_f32 v[4:5], v[182:183], v[66:67], v[4:5] op_sel:[1,0,0]
	v_mov_b32_e32 v6, v185
	v_pk_fma_f32 v[4:5], v[184:185], v[68:69], v[4:5] op_sel_hi:[0,1,1]
	v_pk_fma_f32 v[190:191], v[6:7], v[70:71], v[4:5] op_sel_hi:[0,1,1]
	ds_read_b128 v[4:7], v210 offset:16528
	ds_read_b128 v[182:185], v210 offset:16544
	ds_read_b128 v[186:189], v210 offset:16560
	ds_read_b128 v[192:195], v210 offset:16576
	s_waitcnt lgkmcnt(3)
	v_pk_fma_f32 v[190:191], v[4:5], v[72:73], v[190:191] op_sel_hi:[0,1,1]
	v_pk_fma_f32 v[4:5], v[4:5], v[74:75], v[190:191] op_sel:[1,0,0]
	v_mov_b32_e32 v196, v7
	v_pk_fma_f32 v[4:5], v[6:7], v[76:77], v[4:5] op_sel_hi:[0,1,1]
	v_pk_fma_f32 v[4:5], v[196:197], v[78:79], v[4:5] op_sel_hi:[0,1,1]
	s_waitcnt lgkmcnt(2)
	v_pk_fma_f32 v[4:5], v[182:183], v[80:81], v[4:5] op_sel_hi:[0,1,1]
	v_pk_fma_f32 v[4:5], v[182:183], v[82:83], v[4:5] op_sel:[1,0,0]
	v_mov_b32_e32 v6, v185
	v_pk_fma_f32 v[4:5], v[184:185], v[84:85], v[4:5] op_sel_hi:[0,1,1]
	v_pk_fma_f32 v[4:5], v[6:7], v[86:87], v[4:5] op_sel_hi:[0,1,1]
	s_waitcnt lgkmcnt(1)
	v_pk_fma_f32 v[4:5], v[186:187], v[88:89], v[4:5] op_sel_hi:[0,1,1]
	v_pk_fma_f32 v[4:5], v[186:187], v[90:91], v[4:5] op_sel:[1,0,0]
	v_mov_b32_e32 v6, v189
	v_pk_fma_f32 v[4:5], v[188:189], v[92:93], v[4:5] op_sel_hi:[0,1,1]
	v_pk_fma_f32 v[4:5], v[6:7], v[94:95], v[4:5] op_sel_hi:[0,1,1]
	s_waitcnt lgkmcnt(0)
	v_pk_fma_f32 v[4:5], v[192:193], v[96:97], v[4:5] op_sel_hi:[0,1,1]
	v_pk_fma_f32 v[182:183], v[192:193], v[98:99], v[4:5] op_sel:[1,0,0]
	ds_read_b128 v[4:7], v210 offset:16592
	v_pk_fma_f32 v[182:183], v[194:195], v[100:101], v[182:183] op_sel_hi:[0,1,1]
	v_mov_b32_e32 v184, v195
	v_pk_fma_f32 v[186:187], v[184:185], v[102:103], v[182:183] op_sel_hi:[0,1,1]
	ds_read_b128 v[182:185], v210 offset:16608
	s_waitcnt lgkmcnt(1)
	v_pk_fma_f32 v[186:187], v[4:5], v[104:105], v[186:187] op_sel_hi:[0,1,1]
	v_pk_fma_f32 v[4:5], v[4:5], v[106:107], v[186:187] op_sel:[1,0,0]
	s_nop 0
	v_pk_fma_f32 v[4:5], v[6:7], v[108:109], v[4:5] op_sel_hi:[0,1,1]
	v_mov_b32_e32 v6, v7
	v_pk_fma_f32 v[4:5], v[6:7], v[110:111], v[4:5] op_sel_hi:[0,1,1]
	s_waitcnt lgkmcnt(0)
	v_pk_fma_f32 v[4:5], v[182:183], v[112:113], v[4:5] op_sel_hi:[0,1,1]
	v_pk_fma_f32 v[182:183], v[182:183], v[114:115], v[4:5] op_sel:[1,0,0]
	ds_read_b128 v[4:7], v210 offset:16624
	v_pk_fma_f32 v[182:183], v[184:185], v[116:117], v[182:183] op_sel_hi:[0,1,1]
	v_mov_b32_e32 v184, v185
	v_pk_fma_f32 v[186:187], v[184:185], v[118:119], v[182:183] op_sel_hi:[0,1,1]
	ds_read_b128 v[182:185], v210 offset:16640
	s_waitcnt lgkmcnt(1)
	v_pk_fma_f32 v[186:187], v[4:5], v[120:121], v[186:187] op_sel_hi:[0,1,1]
	v_pk_fma_f32 v[4:5], v[4:5], v[122:123], v[186:187] op_sel:[1,0,0]
	s_nop 0
	v_pk_fma_f32 v[4:5], v[6:7], v[124:125], v[4:5] op_sel_hi:[0,1,1]
	v_mov_b32_e32 v6, v7
	v_pk_fma_f32 v[4:5], v[6:7], v[126:127], v[4:5] op_sel_hi:[0,1,1]
	s_waitcnt lgkmcnt(0)
	v_pk_fma_f32 v[4:5], v[182:183], v[128:129], v[4:5] op_sel_hi:[0,1,1]
	v_pk_fma_f32 v[4:5], v[182:183], v[130:131], v[4:5] op_sel:[1,0,0]
	v_mov_b32_e32 v6, v185
	v_pk_fma_f32 v[4:5], v[184:185], v[132:133], v[4:5] op_sel_hi:[0,1,1]
	v_pk_fma_f32 v[4:5], v[6:7], v[134:135], v[4:5] op_sel_hi:[0,1,1]
	ds_read_b128 v[182:185], v210 offset:24592
	ds_read_b128 v[186:189], v210 offset:24608
	ds_read_b128 v[192:195], v210 offset:24624
	ds_read_b128 v[196:199], v210 offset:24640
	s_waitcnt lgkmcnt(3)
	v_pk_fma_f32 v[6:7], v[182:183], v[8:9], 0 op_sel_hi:[0,1,0]
	v_pk_fma_f32 v[6:7], v[182:183], v[10:11], v[6:7] op_sel:[1,0,0]
	v_mov_b32_e32 v190, v185
	v_pk_fma_f32 v[6:7], v[184:185], v[12:13], v[6:7] op_sel_hi:[0,1,1]
	v_pk_fma_f32 v[6:7], v[190:191], v[14:15], v[6:7] op_sel_hi:[0,1,1]
	s_waitcnt lgkmcnt(2)
	v_pk_fma_f32 v[6:7], v[186:187], v[16:17], v[6:7] op_sel_hi:[0,1,1]
	v_pk_fma_f32 v[6:7], v[186:187], v[18:19], v[6:7] op_sel:[1,0,0]
	v_mov_b32_e32 v182, v189
	v_pk_fma_f32 v[6:7], v[188:189], v[20:21], v[6:7] op_sel_hi:[0,1,1]
	v_pk_fma_f32 v[6:7], v[182:183], v[22:23], v[6:7] op_sel_hi:[0,1,1]
	s_waitcnt lgkmcnt(1)
	v_pk_fma_f32 v[6:7], v[192:193], v[24:25], v[6:7] op_sel_hi:[0,1,1]
	v_pk_fma_f32 v[6:7], v[192:193], v[26:27], v[6:7] op_sel:[1,0,0]
	v_mov_b32_e32 v182, v195
	v_pk_fma_f32 v[6:7], v[194:195], v[28:29], v[6:7] op_sel_hi:[0,1,1]
	v_pk_fma_f32 v[6:7], v[182:183], v[30:31], v[6:7] op_sel_hi:[0,1,1]
	ds_read_b128 v[182:185], v210 offset:24656
	s_waitcnt lgkmcnt(1)
; template <bool DRY = false>
; DI void phase_ln_router(const Params& p, char* smem, int bid, int nb) {
;     ...
;       f32x2_t acc[8];
; #pragma unroll
;       for (int j = 0; j < 8; ++j) acc[j] = (f32x2_t){0.f, 0.f};
; #pragma unroll
;       for (int j = 0; j < 8; ++j) {
; #pragma unroll
;         for (int i4 = 0; i4 < 16; ++i4) {
;           const float4 h = *(const float4*)(hs + j * 2048 + ks * 64 + 4 * i4);
;           acc[j] = __builtin_elementwise_fma((f32x2_t){h.x, h.x}, wr[4 * i4], acc[j]); acc[j] = __builtin_elementwise_fma((f32x2_t){h.y, h.y}, wr[4 * i4 + 1], acc[j]);
;           acc[j] = __builtin_elementwise_fma((f32x2_t){h.z, h.z}, wr[4 * i4 + 2], acc[j]); acc[j] = __builtin_elementwise_fma((f32x2_t){h.w, h.w}, wr[4 * i4 + 3], acc[j]);
;           if ((i4 & 7) == 7) __builtin_amdgcn_sched_barrier(0);
;         }
;       }
	v_pk_fma_f32 v[6:7], v[196:197], v[32:33], v[6:7] op_sel_hi:[0,1,1]
	v_pk_fma_f32 v[6:7], v[196:197], v[34:35], v[6:7] op_sel:[1,0,0]
	v_mov_b32_e32 v186, v199
	v_pk_fma_f32 v[6:7], v[198:199], v[36:37], v[6:7] op_sel_hi:[0,1,1]
	v_pk_fma_f32 v[6:7], v[186:187], v[38:39], v[6:7] op_sel_hi:[0,1,1]
	ds_read_b128 v[186:189], v210 offset:24672
	s_waitcnt lgkmcnt(1)
	v_pk_fma_f32 v[6:7], v[182:183], v[40:41], v[6:7] op_sel_hi:[0,1,1]
	v_pk_fma_f32 v[6:7], v[182:183], v[42:43], v[6:7] op_sel:[1,0,0]
	v_mov_b32_e32 v182, v185
	v_pk_fma_f32 v[6:7], v[184:185], v[44:45], v[6:7] op_sel_hi:[0,1,1]
	v_pk_fma_f32 v[6:7], v[182:183], v[46:47], v[6:7] op_sel_hi:[0,1,1]
	ds_read_b128 v[182:185], v210 offset:24688
	s_waitcnt lgkmcnt(1)
	v_pk_fma_f32 v[6:7], v[186:187], v[48:49], v[6:7] op_sel_hi:[0,1,1]
	v_pk_fma_f32 v[6:7], v[186:187], v[50:51], v[6:7] op_sel:[1,0,0]
	v_mov_b32_e32 v186, v189
	v_pk_fma_f32 v[6:7], v[188:189], v[52:53], v[6:7] op_sel_hi:[0,1,1]
	v_pk_fma_f32 v[6:7], v[186:187], v[54:55], v[6:7] op_sel_hi:[0,1,1]
	ds_read_b128 v[186:189], v210 offset:24704
	s_waitcnt lgkmcnt(1)
	v_pk_fma_f32 v[6:7], v[182:183], v[56:57], v[6:7] op_sel_hi:[0,1,1]
	v_pk_fma_f32 v[6:7], v[182:183], v[58:59], v[6:7] op_sel:[1,0,0]
	v_mov_b32_e32 v182, v185
	v_pk_fma_f32 v[6:7], v[184:185], v[60:61], v[6:7] op_sel_hi:[0,1,1]
	v_pk_fma_f32 v[6:7], v[182:183], v[62:63], v[6:7] op_sel_hi:[0,1,1]
	s_waitcnt lgkmcnt(0)
	v_pk_fma_f32 v[6:7], v[186:187], v[64:65], v[6:7] op_sel_hi:[0,1,1]
	v_pk_fma_f32 v[6:7], v[186:187], v[66:67], v[6:7] op_sel:[1,0,0]
	v_mov_b32_e32 v182, v189
	v_pk_fma_f32 v[6:7], v[188:189], v[68:69], v[6:7] op_sel_hi:[0,1,1]
	v_pk_fma_f32 v[6:7], v[182:183], v[70:71], v[6:7] op_sel_hi:[0,1,1]
	ds_read_b128 v[182:185], v210 offset:24720
	ds_read_b128 v[186:189], v210 offset:24736
	ds_read_b128 v[192:195], v210 offset:24752
	ds_read_b128 v[196:199], v210 offset:24768
	s_waitcnt lgkmcnt(3)
	v_pk_fma_f32 v[6:7], v[182:183], v[72:73], v[6:7] op_sel_hi:[0,1,1]
	v_pk_fma_f32 v[6:7], v[182:183], v[74:75], v[6:7] op_sel:[1,0,0]
	v_mov_b32_e32 v190, v185
	v_pk_fma_f32 v[6:7], v[184:185], v[76:77], v[6:7] op_sel_hi:[0,1,1]
	v_pk_fma_f32 v[6:7], v[190:191], v[78:79], v[6:7] op_sel_hi:[0,1,1]
	s_waitcnt lgkmcnt(2)
	v_pk_fma_f32 v[6:7], v[186:187], v[80:81], v[6:7] op_sel_hi:[0,1,1]
	v_pk_fma_f32 v[6:7], v[186:187], v[82:83], v[6:7] op_sel:[1,0,0]
	v_mov_b32_e32 v182, v189
	v_pk_fma_f32 v[6:7], v[188:189], v[84:85], v[6:7] op_sel_hi:[0,1,1]
	v_pk_fma_f32 v[6:7], v[182:183], v[86:87], v[6:7] op_sel_hi:[0,1,1]
	s_waitcnt lgkmcnt(1)
	v_pk_fma_f32 v[6:7], v[192:193], v[88:89], v[6:7] op_sel_hi:[0,1,1]
	v_pk_fma_f32 v[6:7], v[192:193], v[90:91], v[6:7] op_sel:[1,0,0]
	v_mov_b32_e32 v182, v195
	v_pk_fma_f32 v[6:7], v[194:195], v[92:93], v[6:7] op_sel_hi:[0,1,1]
	v_pk_fma_f32 v[6:7], v[182:183], v[94:95], v[6:7] op_sel_hi:[0,1,1]
	ds_read_b128 v[182:185], v210 offset:24784
	s_waitcnt lgkmcnt(1)
	v_pk_fma_f32 v[6:7], v[196:197], v[96:97], v[6:7] op_sel_hi:[0,1,1]
	v_pk_fma_f32 v[6:7], v[196:197], v[98:99], v[6:7] op_sel:[1,0,0]
	v_mov_b32_e32 v186, v199
	v_pk_fma_f32 v[6:7], v[198:199], v[100:101], v[6:7] op_sel_hi:[0,1,1]
	v_pk_fma_f32 v[6:7], v[186:187], v[102:103], v[6:7] op_sel_hi:[0,1,1]
	ds_read_b128 v[186:189], v210 offset:24800
	s_waitcnt lgkmcnt(1)
	v_pk_fma_f32 v[6:7], v[182:183], v[104:105], v[6:7] op_sel_hi:[0,1,1]
	v_pk_fma_f32 v[6:7], v[182:183], v[106:107], v[6:7] op_sel:[1,0,0]
	v_mov_b32_e32 v182, v185
	v_pk_fma_f32 v[6:7], v[184:185], v[108:109], v[6:7] op_sel_hi:[0,1,1]
	v_pk_fma_f32 v[6:7], v[182:183], v[110:111], v[6:7] op_sel_hi:[0,1,1]
	ds_read_b128 v[182:185], v210 offset:24816
	s_waitcnt lgkmcnt(1)
	v_pk_fma_f32 v[6:7], v[186:187], v[112:113], v[6:7] op_sel_hi:[0,1,1]
	v_pk_fma_f32 v[6:7], v[186:187], v[114:115], v[6:7] op_sel:[1,0,0]
	v_mov_b32_e32 v186, v189
	v_pk_fma_f32 v[6:7], v[188:189], v[116:117], v[6:7] op_sel_hi:[0,1,1]
	v_pk_fma_f32 v[6:7], v[186:187], v[118:119], v[6:7] op_sel_hi:[0,1,1]
	ds_read_b128 v[186:189], v210 offset:24832
	s_waitcnt lgkmcnt(1)
	v_pk_fma_f32 v[6:7], v[182:183], v[120:121], v[6:7] op_sel_hi:[0,1,1]
	v_pk_fma_f32 v[6:7], v[182:183], v[122:123], v[6:7] op_sel:[1,0,0]
	v_mov_b32_e32 v182, v185
	v_pk_fma_f32 v[6:7], v[184:185], v[124:125], v[6:7] op_sel_hi:[0,1,1]
	v_pk_fma_f32 v[6:7], v[182:183], v[126:127], v[6:7] op_sel_hi:[0,1,1]
	s_waitcnt lgkmcnt(0)
	v_pk_fma_f32 v[6:7], v[186:187], v[128:129], v[6:7] op_sel_hi:[0,1,1]
	v_pk_fma_f32 v[6:7], v[186:187], v[130:131], v[6:7] op_sel:[1,0,0]
	v_mov_b32_e32 v182, v189
	v_pk_fma_f32 v[6:7], v[188:189], v[132:133], v[6:7] op_sel_hi:[0,1,1]
	v_pk_fma_f32 v[6:7], v[182:183], v[134:135], v[6:7] op_sel_hi:[0,1,1]
	ds_read_b128 v[182:185], v210 offset:32784
	ds_read_b128 v[186:189], v210 offset:32800
	ds_read_b128 v[192:195], v210 offset:32816
	ds_read_b128 v[196:199], v210 offset:32832
	s_waitcnt lgkmcnt(3)
	v_pk_fma_f32 v[190:191], v[182:183], v[8:9], 0 op_sel_hi:[0,1,0]
	v_pk_fma_f32 v[182:183], v[182:183], v[10:11], v[190:191] op_sel:[1,0,0]
	v_mov_b32_e32 v222, v185
	v_pk_fma_f32 v[182:183], v[184:185], v[12:13], v[182:183] op_sel_hi:[0,1,1]
	v_pk_fma_f32 v[182:183], v[222:223], v[14:15], v[182:183] op_sel_hi:[0,1,1]
	s_waitcnt lgkmcnt(2)
	v_pk_fma_f32 v[182:183], v[186:187], v[16:17], v[182:183] op_sel_hi:[0,1,1]
	v_pk_fma_f32 v[182:183], v[186:187], v[18:19], v[182:183] op_sel:[1,0,0]
	v_mov_b32_e32 v184, v189
	v_pk_fma_f32 v[182:183], v[188:189], v[20:21], v[182:183] op_sel_hi:[0,1,1]
	v_pk_fma_f32 v[182:183], v[184:185], v[22:23], v[182:183] op_sel_hi:[0,1,1]
	s_waitcnt lgkmcnt(1)
; template <bool DRY = false>
; DI void phase_ln_router(const Params& p, char* smem, int bid, int nb) {
;     ...
;       f32x2_t acc[8];
; #pragma unroll
;       for (int j = 0; j < 8; ++j) acc[j] = (f32x2_t){0.f, 0.f};
; #pragma unroll
;       for (int j = 0; j < 8; ++j) {
; #pragma unroll
;         for (int i4 = 0; i4 < 16; ++i4) {
;           const float4 h = *(const float4*)(hs + j * 2048 + ks * 64 + 4 * i4);
;           acc[j] = __builtin_elementwise_fma((f32x2_t){h.x, h.x}, wr[4 * i4], acc[j]); acc[j] = __builtin_elementwise_fma((f32x2_t){h.y, h.y}, wr[4 * i4 + 1], acc[j]);
;           acc[j] = __builtin_elementwise_fma((f32x2_t){h.z, h.z}, wr[4 * i4 + 2], acc[j]); acc[j] = __builtin_elementwise_fma((f32x2_t){h.w, h.w}, wr[4 * i4 + 3], acc[j]);
;           if ((i4 & 7) == 7) __builtin_amdgcn_sched_barrier(0);
;         }
;       }
	v_pk_fma_f32 v[182:183], v[192:193], v[24:25], v[182:183] op_sel_hi:[0,1,1]
	v_pk_fma_f32 v[182:183], v[192:193], v[26:27], v[182:183] op_sel:[1,0,0]
	v_mov_b32_e32 v184, v195
	v_pk_fma_f32 v[182:183], v[194:195], v[28:29], v[182:183] op_sel_hi:[0,1,1]
	v_pk_fma_f32 v[182:183], v[184:185], v[30:31], v[182:183] op_sel_hi:[0,1,1]
	s_waitcnt lgkmcnt(0)
	v_pk_fma_f32 v[182:183], v[196:197], v[32:33], v[182:183] op_sel_hi:[0,1,1]
	v_pk_fma_f32 v[186:187], v[196:197], v[34:35], v[182:183] op_sel:[1,0,0]
	ds_read_b128 v[182:185], v210 offset:32848
	v_pk_fma_f32 v[186:187], v[198:199], v[36:37], v[186:187] op_sel_hi:[0,1,1]
	v_mov_b32_e32 v188, v199
	v_pk_fma_f32 v[190:191], v[188:189], v[38:39], v[186:187] op_sel_hi:[0,1,1]
	ds_read_b128 v[186:189], v210 offset:32864
	s_waitcnt lgkmcnt(1)
	v_pk_fma_f32 v[190:191], v[182:183], v[40:41], v[190:191] op_sel_hi:[0,1,1]
	v_pk_fma_f32 v[182:183], v[182:183], v[42:43], v[190:191] op_sel:[1,0,0]
	s_nop 0
	v_pk_fma_f32 v[182:183], v[184:185], v[44:45], v[182:183] op_sel_hi:[0,1,1]
	v_mov_b32_e32 v184, v185
	v_pk_fma_f32 v[182:183], v[184:185], v[46:47], v[182:183] op_sel_hi:[0,1,1]
	s_waitcnt lgkmcnt(0)
	v_pk_fma_f32 v[182:183], v[186:187], v[48:49], v[182:183] op_sel_hi:[0,1,1]
	v_pk_fma_f32 v[186:187], v[186:187], v[50:51], v[182:183] op_sel:[1,0,0]
	ds_read_b128 v[182:185], v210 offset:32880
	v_pk_fma_f32 v[186:187], v[188:189], v[52:53], v[186:187] op_sel_hi:[0,1,1]
	v_mov_b32_e32 v188, v189
	v_pk_fma_f32 v[190:191], v[188:189], v[54:55], v[186:187] op_sel_hi:[0,1,1]
	ds_read_b128 v[186:189], v210 offset:32896
	s_waitcnt lgkmcnt(1)
	v_pk_fma_f32 v[190:191], v[182:183], v[56:57], v[190:191] op_sel_hi:[0,1,1]
	v_pk_fma_f32 v[182:183], v[182:183], v[58:59], v[190:191] op_sel:[1,0,0]
	s_nop 0
	v_pk_fma_f32 v[182:183], v[184:185], v[60:61], v[182:183] op_sel_hi:[0,1,1]
	v_mov_b32_e32 v184, v185
	v_pk_fma_f32 v[182:183], v[184:185], v[62:63], v[182:183] op_sel_hi:[0,1,1]
	s_waitcnt lgkmcnt(0)
	v_pk_fma_f32 v[182:183], v[186:187], v[64:65], v[182:183] op_sel_hi:[0,1,1]
	v_pk_fma_f32 v[182:183], v[186:187], v[66:67], v[182:183] op_sel:[1,0,0]
	v_mov_b32_e32 v184, v189
	v_pk_fma_f32 v[182:183], v[188:189], v[68:69], v[182:183] op_sel_hi:[0,1,1]
	v_pk_fma_f32 v[190:191], v[184:185], v[70:71], v[182:183] op_sel_hi:[0,1,1]
	ds_read_b128 v[182:185], v210 offset:32912
	ds_read_b128 v[186:189], v210 offset:32928
	ds_read_b128 v[192:195], v210 offset:32944
	ds_read_b128 v[196:199], v210 offset:32960
	s_waitcnt lgkmcnt(3)
	v_pk_fma_f32 v[190:191], v[182:183], v[72:73], v[190:191] op_sel_hi:[0,1,1]
	v_pk_fma_f32 v[182:183], v[182:183], v[74:75], v[190:191] op_sel:[1,0,0]
	v_mov_b32_e32 v222, v185
	v_pk_fma_f32 v[182:183], v[184:185], v[76:77], v[182:183] op_sel_hi:[0,1,1]
	v_pk_fma_f32 v[182:183], v[222:223], v[78:79], v[182:183] op_sel_hi:[0,1,1]
	s_waitcnt lgkmcnt(2)
	v_pk_fma_f32 v[182:183], v[186:187], v[80:81], v[182:183] op_sel_hi:[0,1,1]
	v_pk_fma_f32 v[182:183], v[186:187], v[82:83], v[182:183] op_sel:[1,0,0]
	v_mov_b32_e32 v184, v189
	v_pk_fma_f32 v[182:183], v[188:189], v[84:85], v[182:183] op_sel_hi:[0,1,1]
	v_pk_fma_f32 v[182:183], v[184:185], v[86:87], v[182:183] op_sel_hi:[0,1,1]
	s_waitcnt lgkmcnt(1)
	v_pk_fma_f32 v[182:183], v[192:193], v[88:89], v[182:183] op_sel_hi:[0,1,1]
	v_pk_fma_f32 v[182:183], v[192:193], v[90:91], v[182:183] op_sel:[1,0,0]
	v_mov_b32_e32 v184, v195
	v_pk_fma_f32 v[182:183], v[194:195], v[92:93], v[182:183] op_sel_hi:[0,1,1]
	v_pk_fma_f32 v[182:183], v[184:185], v[94:95], v[182:183] op_sel_hi:[0,1,1]
	s_waitcnt lgkmcnt(0)
	v_pk_fma_f32 v[182:183], v[196:197], v[96:97], v[182:183] op_sel_hi:[0,1,1]
	v_pk_fma_f32 v[186:187], v[196:197], v[98:99], v[182:183] op_sel:[1,0,0]
	ds_read_b128 v[182:185], v210 offset:32976
	v_pk_fma_f32 v[186:187], v[198:199], v[100:101], v[186:187] op_sel_hi:[0,1,1]
	v_mov_b32_e32 v188, v199
	v_pk_fma_f32 v[190:191], v[188:189], v[102:103], v[186:187] op_sel_hi:[0,1,1]
	ds_read_b128 v[186:189], v210 offset:32992
	s_waitcnt lgkmcnt(1)
	v_pk_fma_f32 v[190:191], v[182:183], v[104:105], v[190:191] op_sel_hi:[0,1,1]
	v_pk_fma_f32 v[182:183], v[182:183], v[106:107], v[190:191] op_sel:[1,0,0]
	s_nop 0
	v_pk_fma_f32 v[182:183], v[184:185], v[108:109], v[182:183] op_sel_hi:[0,1,1]
	v_mov_b32_e32 v184, v185
	v_pk_fma_f32 v[182:183], v[184:185], v[110:111], v[182:183] op_sel_hi:[0,1,1]
	s_waitcnt lgkmcnt(0)
	v_pk_fma_f32 v[182:183], v[186:187], v[112:113], v[182:183] op_sel_hi:[0,1,1]
	v_pk_fma_f32 v[186:187], v[186:187], v[114:115], v[182:183] op_sel:[1,0,0]
	ds_read_b128 v[182:185], v210 offset:33008
	v_pk_fma_f32 v[186:187], v[188:189], v[116:117], v[186:187] op_sel_hi:[0,1,1]
	v_mov_b32_e32 v188, v189
	v_pk_fma_f32 v[190:191], v[188:189], v[118:119], v[186:187] op_sel_hi:[0,1,1]
	ds_read_b128 v[186:189], v210 offset:33024
	s_waitcnt lgkmcnt(1)
	v_pk_fma_f32 v[190:191], v[182:183], v[120:121], v[190:191] op_sel_hi:[0,1,1]
	v_pk_fma_f32 v[182:183], v[182:183], v[122:123], v[190:191] op_sel:[1,0,0]
	s_nop 0
	v_pk_fma_f32 v[182:183], v[184:185], v[124:125], v[182:183] op_sel_hi:[0,1,1]
	v_mov_b32_e32 v184, v185
	v_pk_fma_f32 v[182:183], v[184:185], v[126:127], v[182:183] op_sel_hi:[0,1,1]
	s_waitcnt lgkmcnt(0)
	v_pk_fma_f32 v[182:183], v[186:187], v[128:129], v[182:183] op_sel_hi:[0,1,1]
	v_pk_fma_f32 v[182:183], v[186:187], v[130:131], v[182:183] op_sel:[1,0,0]
	v_mov_b32_e32 v184, v189
	v_pk_fma_f32 v[182:183], v[188:189], v[132:133], v[182:183] op_sel_hi:[0,1,1]
	v_pk_fma_f32 v[182:183], v[184:185], v[134:135], v[182:183] op_sel_hi:[0,1,1]
	ds_read_b128 v[184:187], v210 offset:40976
	ds_read_b128 v[192:195], v210 offset:40992
	ds_read_b128 v[196:199], v210 offset:41008
	ds_read_b128 v[222:225], v210 offset:41024
	s_waitcnt lgkmcnt(3)
; template <bool DRY = false>
; DI void phase_ln_router(const Params& p, char* smem, int bid, int nb) {
;     ...
;       f32x2_t acc[8];
; #pragma unroll
;       for (int j = 0; j < 8; ++j) acc[j] = (f32x2_t){0.f, 0.f};
; #pragma unroll
;       for (int j = 0; j < 8; ++j) {
; #pragma unroll
;         for (int i4 = 0; i4 < 16; ++i4) {
;           const float4 h = *(const float4*)(hs + j * 2048 + ks * 64 + 4 * i4);
;           acc[j] = __builtin_elementwise_fma((f32x2_t){h.x, h.x}, wr[4 * i4], acc[j]); acc[j] = __builtin_elementwise_fma((f32x2_t){h.y, h.y}, wr[4 * i4 + 1], acc[j]);
;           acc[j] = __builtin_elementwise_fma((f32x2_t){h.z, h.z}, wr[4 * i4 + 2], acc[j]); acc[j] = __builtin_elementwise_fma((f32x2_t){h.w, h.w}, wr[4 * i4 + 3], acc[j]);
;           if ((i4 & 7) == 7) __builtin_amdgcn_sched_barrier(0);
;         }
;       }
	v_pk_fma_f32 v[188:189], v[184:185], v[8:9], 0 op_sel_hi:[0,1,0]
	v_pk_fma_f32 v[184:185], v[184:185], v[10:11], v[188:189] op_sel:[1,0,0]
	v_mov_b32_e32 v190, v187
	v_pk_fma_f32 v[184:185], v[186:187], v[12:13], v[184:185] op_sel_hi:[0,1,1]
	v_pk_fma_f32 v[184:185], v[190:191], v[14:15], v[184:185] op_sel_hi:[0,1,1]
	s_waitcnt lgkmcnt(2)
	v_pk_fma_f32 v[184:185], v[192:193], v[16:17], v[184:185] op_sel_hi:[0,1,1]
	v_pk_fma_f32 v[184:185], v[192:193], v[18:19], v[184:185] op_sel:[1,0,0]
	v_mov_b32_e32 v186, v195
	v_pk_fma_f32 v[184:185], v[194:195], v[20:21], v[184:185] op_sel_hi:[0,1,1]
	v_pk_fma_f32 v[184:185], v[186:187], v[22:23], v[184:185] op_sel_hi:[0,1,1]
	s_waitcnt lgkmcnt(1)
	v_pk_fma_f32 v[184:185], v[196:197], v[24:25], v[184:185] op_sel_hi:[0,1,1]
	v_pk_fma_f32 v[184:185], v[196:197], v[26:27], v[184:185] op_sel:[1,0,0]
	v_mov_b32_e32 v186, v199
	v_pk_fma_f32 v[184:185], v[198:199], v[28:29], v[184:185] op_sel_hi:[0,1,1]
	v_pk_fma_f32 v[184:185], v[186:187], v[30:31], v[184:185] op_sel_hi:[0,1,1]
	s_waitcnt lgkmcnt(0)
	v_pk_fma_f32 v[184:185], v[222:223], v[32:33], v[184:185] op_sel_hi:[0,1,1]
	v_pk_fma_f32 v[188:189], v[222:223], v[34:35], v[184:185] op_sel:[1,0,0]
	ds_read_b128 v[184:187], v210 offset:41040
	ds_read_b128 v[192:195], v210 offset:41056
	v_pk_fma_f32 v[188:189], v[224:225], v[36:37], v[188:189] op_sel_hi:[0,1,1]
	v_mov_b32_e32 v190, v225
	v_pk_fma_f32 v[188:189], v[190:191], v[38:39], v[188:189] op_sel_hi:[0,1,1]
	s_waitcnt lgkmcnt(1)
	v_pk_fma_f32 v[188:189], v[184:185], v[40:41], v[188:189] op_sel_hi:[0,1,1]
	v_pk_fma_f32 v[184:185], v[184:185], v[42:43], v[188:189] op_sel:[1,0,0]
	s_waitcnt lgkmcnt(0)
	v_mov_b32_e32 v190, v195
	v_pk_fma_f32 v[184:185], v[186:187], v[44:45], v[184:185] op_sel_hi:[0,1,1]
	v_mov_b32_e32 v186, v187
	v_pk_fma_f32 v[184:185], v[186:187], v[46:47], v[184:185] op_sel_hi:[0,1,1]
	v_pk_fma_f32 v[184:185], v[192:193], v[48:49], v[184:185] op_sel_hi:[0,1,1]
	v_pk_fma_f32 v[188:189], v[192:193], v[50:51], v[184:185] op_sel:[1,0,0]
	ds_read_b128 v[184:187], v210 offset:41072
	v_pk_fma_f32 v[188:189], v[194:195], v[52:53], v[188:189] op_sel_hi:[0,1,1]
	v_pk_fma_f32 v[188:189], v[190:191], v[54:55], v[188:189] op_sel_hi:[0,1,1]
	ds_read_b128 v[192:195], v210 offset:41088
	s_waitcnt lgkmcnt(1)
	v_pk_fma_f32 v[188:189], v[184:185], v[56:57], v[188:189] op_sel_hi:[0,1,1]
	v_pk_fma_f32 v[184:185], v[184:185], v[58:59], v[188:189] op_sel:[1,0,0]
	s_nop 0
	v_pk_fma_f32 v[184:185], v[186:187], v[60:61], v[184:185] op_sel_hi:[0,1,1]
	v_mov_b32_e32 v186, v187
	v_pk_fma_f32 v[184:185], v[186:187], v[62:63], v[184:185] op_sel_hi:[0,1,1]
	s_waitcnt lgkmcnt(0)
	v_pk_fma_f32 v[184:185], v[192:193], v[64:65], v[184:185] op_sel_hi:[0,1,1]
	v_pk_fma_f32 v[184:185], v[192:193], v[66:67], v[184:185] op_sel:[1,0,0]
	v_mov_b32_e32 v186, v195
	v_pk_fma_f32 v[184:185], v[194:195], v[68:69], v[184:185] op_sel_hi:[0,1,1]
	v_pk_fma_f32 v[188:189], v[186:187], v[70:71], v[184:185] op_sel_hi:[0,1,1]
	ds_read_b128 v[184:187], v210 offset:41104
	ds_read_b128 v[192:195], v210 offset:41120
	ds_read_b128 v[196:199], v210 offset:41136
	ds_read_b128 v[222:225], v210 offset:41152
	s_waitcnt lgkmcnt(3)
	v_pk_fma_f32 v[188:189], v[184:185], v[72:73], v[188:189] op_sel_hi:[0,1,1]
	v_pk_fma_f32 v[184:185], v[184:185], v[74:75], v[188:189] op_sel:[1,0,0]
	v_mov_b32_e32 v190, v187
	v_pk_fma_f32 v[184:185], v[186:187], v[76:77], v[184:185] op_sel_hi:[0,1,1]
	v_pk_fma_f32 v[184:185], v[190:191], v[78:79], v[184:185] op_sel_hi:[0,1,1]
	s_waitcnt lgkmcnt(2)
	v_pk_fma_f32 v[184:185], v[192:193], v[80:81], v[184:185] op_sel_hi:[0,1,1]
	v_pk_fma_f32 v[184:185], v[192:193], v[82:83], v[184:185] op_sel:[1,0,0]
	v_mov_b32_e32 v186, v195
	v_pk_fma_f32 v[184:185], v[194:195], v[84:85], v[184:185] op_sel_hi:[0,1,1]
	v_pk_fma_f32 v[184:185], v[186:187], v[86:87], v[184:185] op_sel_hi:[0,1,1]
	s_waitcnt lgkmcnt(1)
	v_pk_fma_f32 v[184:185], v[196:197], v[88:89], v[184:185] op_sel_hi:[0,1,1]
	v_pk_fma_f32 v[184:185], v[196:197], v[90:91], v[184:185] op_sel:[1,0,0]
	v_mov_b32_e32 v186, v199
	v_pk_fma_f32 v[184:185], v[198:199], v[92:93], v[184:185] op_sel_hi:[0,1,1]
	v_pk_fma_f32 v[184:185], v[186:187], v[94:95], v[184:185] op_sel_hi:[0,1,1]
	s_waitcnt lgkmcnt(0)
	v_pk_fma_f32 v[184:185], v[222:223], v[96:97], v[184:185] op_sel_hi:[0,1,1]
	v_pk_fma_f32 v[188:189], v[222:223], v[98:99], v[184:185] op_sel:[1,0,0]
	ds_read_b128 v[184:187], v210 offset:41168
	ds_read_b128 v[192:195], v210 offset:41184
	v_pk_fma_f32 v[188:189], v[224:225], v[100:101], v[188:189] op_sel_hi:[0,1,1]
	v_mov_b32_e32 v190, v225
	v_pk_fma_f32 v[188:189], v[190:191], v[102:103], v[188:189] op_sel_hi:[0,1,1]
	s_waitcnt lgkmcnt(1)
	v_pk_fma_f32 v[188:189], v[184:185], v[104:105], v[188:189] op_sel_hi:[0,1,1]
	v_pk_fma_f32 v[184:185], v[184:185], v[106:107], v[188:189] op_sel:[1,0,0]
	s_waitcnt lgkmcnt(0)
	v_mov_b32_e32 v190, v195
	v_pk_fma_f32 v[184:185], v[186:187], v[108:109], v[184:185] op_sel_hi:[0,1,1]
	v_mov_b32_e32 v186, v187
	v_pk_fma_f32 v[184:185], v[186:187], v[110:111], v[184:185] op_sel_hi:[0,1,1]
	v_pk_fma_f32 v[184:185], v[192:193], v[112:113], v[184:185] op_sel_hi:[0,1,1]
	v_pk_fma_f32 v[188:189], v[192:193], v[114:115], v[184:185] op_sel:[1,0,0]
	ds_read_b128 v[184:187], v210 offset:41200
	v_pk_fma_f32 v[188:189], v[194:195], v[116:117], v[188:189] op_sel_hi:[0,1,1]
	v_pk_fma_f32 v[188:189], v[190:191], v[118:119], v[188:189] op_sel_hi:[0,1,1]
	ds_read_b128 v[192:195], v210 offset:41216
	s_waitcnt lgkmcnt(1)
; template <bool DRY = false>
; DI void phase_ln_router(const Params& p, char* smem, int bid, int nb) {
;     ...
;       f32x2_t acc[8];
; #pragma unroll
;       for (int j = 0; j < 8; ++j) acc[j] = (f32x2_t){0.f, 0.f};
; #pragma unroll
;       for (int j = 0; j < 8; ++j) {
; #pragma unroll
;         for (int i4 = 0; i4 < 16; ++i4) {
;           const float4 h = *(const float4*)(hs + j * 2048 + ks * 64 + 4 * i4);
;           acc[j] = __builtin_elementwise_fma((f32x2_t){h.x, h.x}, wr[4 * i4], acc[j]); acc[j] = __builtin_elementwise_fma((f32x2_t){h.y, h.y}, wr[4 * i4 + 1], acc[j]);
;           acc[j] = __builtin_elementwise_fma((f32x2_t){h.z, h.z}, wr[4 * i4 + 2], acc[j]); acc[j] = __builtin_elementwise_fma((f32x2_t){h.w, h.w}, wr[4 * i4 + 3], acc[j]);
;           if ((i4 & 7) == 7) __builtin_amdgcn_sched_barrier(0);
;         }
;       }
	v_pk_fma_f32 v[188:189], v[184:185], v[120:121], v[188:189] op_sel_hi:[0,1,1]
	v_pk_fma_f32 v[184:185], v[184:185], v[122:123], v[188:189] op_sel:[1,0,0]
	s_nop 0
	v_pk_fma_f32 v[184:185], v[186:187], v[124:125], v[184:185] op_sel_hi:[0,1,1]
	v_mov_b32_e32 v186, v187
	v_pk_fma_f32 v[184:185], v[186:187], v[126:127], v[184:185] op_sel_hi:[0,1,1]
	s_waitcnt lgkmcnt(0)
	v_pk_fma_f32 v[184:185], v[192:193], v[128:129], v[184:185] op_sel_hi:[0,1,1]
	v_pk_fma_f32 v[184:185], v[192:193], v[130:131], v[184:185] op_sel:[1,0,0]
	v_mov_b32_e32 v186, v195
	v_pk_fma_f32 v[184:185], v[194:195], v[132:133], v[184:185] op_sel_hi:[0,1,1]
	v_pk_fma_f32 v[184:185], v[186:187], v[134:135], v[184:185] op_sel_hi:[0,1,1]
	ds_read_b128 v[186:189], v210 offset:49168
	ds_read_b128 v[192:195], v210 offset:49184
	ds_read_b128 v[196:199], v210 offset:49200
	ds_read_b128 v[222:225], v210 offset:49216
	s_waitcnt lgkmcnt(3)
	v_pk_fma_f32 v[190:191], v[186:187], v[8:9], 0 op_sel_hi:[0,1,0]
	v_pk_fma_f32 v[186:187], v[186:187], v[10:11], v[190:191] op_sel:[1,0,0]
	v_mov_b32_e32 v226, v189
	v_pk_fma_f32 v[186:187], v[188:189], v[12:13], v[186:187] op_sel_hi:[0,1,1]
	v_pk_fma_f32 v[186:187], v[226:227], v[14:15], v[186:187] op_sel_hi:[0,1,1]
	s_waitcnt lgkmcnt(2)
	v_pk_fma_f32 v[186:187], v[192:193], v[16:17], v[186:187] op_sel_hi:[0,1,1]
	v_pk_fma_f32 v[186:187], v[192:193], v[18:19], v[186:187] op_sel:[1,0,0]
	v_mov_b32_e32 v188, v195
	v_pk_fma_f32 v[186:187], v[194:195], v[20:21], v[186:187] op_sel_hi:[0,1,1]
	v_pk_fma_f32 v[186:187], v[188:189], v[22:23], v[186:187] op_sel_hi:[0,1,1]
	s_waitcnt lgkmcnt(1)
	v_pk_fma_f32 v[186:187], v[196:197], v[24:25], v[186:187] op_sel_hi:[0,1,1]
	v_pk_fma_f32 v[186:187], v[196:197], v[26:27], v[186:187] op_sel:[1,0,0]
	v_mov_b32_e32 v188, v199
	v_pk_fma_f32 v[186:187], v[198:199], v[28:29], v[186:187] op_sel_hi:[0,1,1]
	v_pk_fma_f32 v[186:187], v[188:189], v[30:31], v[186:187] op_sel_hi:[0,1,1]
	s_waitcnt lgkmcnt(0)
	v_pk_fma_f32 v[186:187], v[222:223], v[32:33], v[186:187] op_sel_hi:[0,1,1]
	v_pk_fma_f32 v[190:191], v[222:223], v[34:35], v[186:187] op_sel:[1,0,0]
	ds_read_b128 v[186:189], v210 offset:49232
	v_pk_fma_f32 v[190:191], v[224:225], v[36:37], v[190:191] op_sel_hi:[0,1,1]
	v_mov_b32_e32 v192, v225
	v_pk_fma_f32 v[190:191], v[192:193], v[38:39], v[190:191] op_sel_hi:[0,1,1]
	ds_read_b128 v[192:195], v210 offset:49248
	s_waitcnt lgkmcnt(1)
	v_pk_fma_f32 v[190:191], v[186:187], v[40:41], v[190:191] op_sel_hi:[0,1,1]
	v_pk_fma_f32 v[186:187], v[186:187], v[42:43], v[190:191] op_sel:[1,0,0]
	s_nop 0
	v_pk_fma_f32 v[186:187], v[188:189], v[44:45], v[186:187] op_sel_hi:[0,1,1]
	v_mov_b32_e32 v188, v189
	v_pk_fma_f32 v[186:187], v[188:189], v[46:47], v[186:187] op_sel_hi:[0,1,1]
	s_waitcnt lgkmcnt(0)
	v_pk_fma_f32 v[186:187], v[192:193], v[48:49], v[186:187] op_sel_hi:[0,1,1]
	v_pk_fma_f32 v[190:191], v[192:193], v[50:51], v[186:187] op_sel:[1,0,0]
	ds_read_b128 v[186:189], v210 offset:49264
	v_pk_fma_f32 v[190:191], v[194:195], v[52:53], v[190:191] op_sel_hi:[0,1,1]
	v_mov_b32_e32 v192, v195
	v_pk_fma_f32 v[190:191], v[192:193], v[54:55], v[190:191] op_sel_hi:[0,1,1]
	ds_read_b128 v[192:195], v210 offset:49280
	s_waitcnt lgkmcnt(1)
	v_pk_fma_f32 v[190:191], v[186:187], v[56:57], v[190:191] op_sel_hi:[0,1,1]
	v_pk_fma_f32 v[186:187], v[186:187], v[58:59], v[190:191] op_sel:[1,0,0]
	s_nop 0
	v_pk_fma_f32 v[186:187], v[188:189], v[60:61], v[186:187] op_sel_hi:[0,1,1]
	v_mov_b32_e32 v188, v189
	v_pk_fma_f32 v[186:187], v[188:189], v[62:63], v[186:187] op_sel_hi:[0,1,1]
	s_waitcnt lgkmcnt(0)
	v_pk_fma_f32 v[186:187], v[192:193], v[64:65], v[186:187] op_sel_hi:[0,1,1]
	v_pk_fma_f32 v[186:187], v[192:193], v[66:67], v[186:187] op_sel:[1,0,0]
	v_mov_b32_e32 v188, v195
	v_pk_fma_f32 v[186:187], v[194:195], v[68:69], v[186:187] op_sel_hi:[0,1,1]
	v_pk_fma_f32 v[190:191], v[188:189], v[70:71], v[186:187] op_sel_hi:[0,1,1]
	ds_read_b128 v[186:189], v210 offset:49296
	ds_read_b128 v[192:195], v210 offset:49312
	ds_read_b128 v[196:199], v210 offset:49328
	ds_read_b128 v[222:225], v210 offset:49344
	s_waitcnt lgkmcnt(3)
	v_pk_fma_f32 v[190:191], v[186:187], v[72:73], v[190:191] op_sel_hi:[0,1,1]
	v_pk_fma_f32 v[186:187], v[186:187], v[74:75], v[190:191] op_sel:[1,0,0]
	v_mov_b32_e32 v226, v189
	v_pk_fma_f32 v[186:187], v[188:189], v[76:77], v[186:187] op_sel_hi:[0,1,1]
	v_pk_fma_f32 v[186:187], v[226:227], v[78:79], v[186:187] op_sel_hi:[0,1,1]
	s_waitcnt lgkmcnt(2)
	v_pk_fma_f32 v[186:187], v[192:193], v[80:81], v[186:187] op_sel_hi:[0,1,1]
	v_pk_fma_f32 v[186:187], v[192:193], v[82:83], v[186:187] op_sel:[1,0,0]
	v_mov_b32_e32 v188, v195
	v_pk_fma_f32 v[186:187], v[194:195], v[84:85], v[186:187] op_sel_hi:[0,1,1]
	v_pk_fma_f32 v[186:187], v[188:189], v[86:87], v[186:187] op_sel_hi:[0,1,1]
	s_waitcnt lgkmcnt(1)
	v_pk_fma_f32 v[186:187], v[196:197], v[88:89], v[186:187] op_sel_hi:[0,1,1]
	v_pk_fma_f32 v[186:187], v[196:197], v[90:91], v[186:187] op_sel:[1,0,0]
	v_mov_b32_e32 v188, v199
	v_pk_fma_f32 v[186:187], v[198:199], v[92:93], v[186:187] op_sel_hi:[0,1,1]
	v_pk_fma_f32 v[186:187], v[188:189], v[94:95], v[186:187] op_sel_hi:[0,1,1]
	s_waitcnt lgkmcnt(0)
	v_pk_fma_f32 v[186:187], v[222:223], v[96:97], v[186:187] op_sel_hi:[0,1,1]
	v_pk_fma_f32 v[190:191], v[222:223], v[98:99], v[186:187] op_sel:[1,0,0]
	ds_read_b128 v[186:189], v210 offset:49360
	v_pk_fma_f32 v[190:191], v[224:225], v[100:101], v[190:191] op_sel_hi:[0,1,1]
	v_mov_b32_e32 v192, v225
	v_pk_fma_f32 v[190:191], v[192:193], v[102:103], v[190:191] op_sel_hi:[0,1,1]
	ds_read_b128 v[192:195], v210 offset:49376
	s_waitcnt lgkmcnt(1)
; template <bool DRY = false>
; DI void phase_ln_router(const Params& p, char* smem, int bid, int nb) {
;     ...
;       f32x2_t acc[8];
; #pragma unroll
;       for (int j = 0; j < 8; ++j) acc[j] = (f32x2_t){0.f, 0.f};
; #pragma unroll
;       for (int j = 0; j < 8; ++j) {
; #pragma unroll
;         for (int i4 = 0; i4 < 16; ++i4) {
;           const float4 h = *(const float4*)(hs + j * 2048 + ks * 64 + 4 * i4);
;           acc[j] = __builtin_elementwise_fma((f32x2_t){h.x, h.x}, wr[4 * i4], acc[j]); acc[j] = __builtin_elementwise_fma((f32x2_t){h.y, h.y}, wr[4 * i4 + 1], acc[j]);
;           acc[j] = __builtin_elementwise_fma((f32x2_t){h.z, h.z}, wr[4 * i4 + 2], acc[j]); acc[j] = __builtin_elementwise_fma((f32x2_t){h.w, h.w}, wr[4 * i4 + 3], acc[j]);
;           if ((i4 & 7) == 7) __builtin_amdgcn_sched_barrier(0);
;         }
;       }
	v_pk_fma_f32 v[190:191], v[186:187], v[104:105], v[190:191] op_sel_hi:[0,1,1]
	v_pk_fma_f32 v[186:187], v[186:187], v[106:107], v[190:191] op_sel:[1,0,0]
	s_nop 0
	v_pk_fma_f32 v[186:187], v[188:189], v[108:109], v[186:187] op_sel_hi:[0,1,1]
	v_mov_b32_e32 v188, v189
	v_pk_fma_f32 v[186:187], v[188:189], v[110:111], v[186:187] op_sel_hi:[0,1,1]
	s_waitcnt lgkmcnt(0)
	v_pk_fma_f32 v[186:187], v[192:193], v[112:113], v[186:187] op_sel_hi:[0,1,1]
	v_pk_fma_f32 v[190:191], v[192:193], v[114:115], v[186:187] op_sel:[1,0,0]
	ds_read_b128 v[186:189], v210 offset:49392
	v_pk_fma_f32 v[190:191], v[194:195], v[116:117], v[190:191] op_sel_hi:[0,1,1]
	v_mov_b32_e32 v192, v195
	v_pk_fma_f32 v[190:191], v[192:193], v[118:119], v[190:191] op_sel_hi:[0,1,1]
	ds_read_b128 v[192:195], v210 offset:49408
	s_waitcnt lgkmcnt(1)
	v_pk_fma_f32 v[190:191], v[186:187], v[120:121], v[190:191] op_sel_hi:[0,1,1]
	v_pk_fma_f32 v[186:187], v[186:187], v[122:123], v[190:191] op_sel:[1,0,0]
	s_nop 0
	v_pk_fma_f32 v[186:187], v[188:189], v[124:125], v[186:187] op_sel_hi:[0,1,1]
	v_mov_b32_e32 v188, v189
	v_pk_fma_f32 v[186:187], v[188:189], v[126:127], v[186:187] op_sel_hi:[0,1,1]
	s_waitcnt lgkmcnt(0)
	v_pk_fma_f32 v[186:187], v[192:193], v[128:129], v[186:187] op_sel_hi:[0,1,1]
	v_pk_fma_f32 v[186:187], v[192:193], v[130:131], v[186:187] op_sel:[1,0,0]
	v_mov_b32_e32 v188, v195
	v_pk_fma_f32 v[186:187], v[194:195], v[132:133], v[186:187] op_sel_hi:[0,1,1]
	v_pk_fma_f32 v[190:191], v[188:189], v[134:135], v[186:187] op_sel_hi:[0,1,1]
	ds_read_b128 v[186:189], v210 offset:57360
	ds_read_b128 v[192:195], v210 offset:57376
	ds_read_b128 v[196:199], v210 offset:57392
	ds_read_b128 v[222:225], v210 offset:57408
	s_waitcnt lgkmcnt(3)
	v_pk_fma_f32 v[226:227], v[186:187], v[8:9], 0 op_sel_hi:[0,1,0]
	v_pk_fma_f32 v[186:187], v[186:187], v[10:11], v[226:227] op_sel:[1,0,0]
	v_mov_b32_e32 v228, v189
	v_pk_fma_f32 v[186:187], v[188:189], v[12:13], v[186:187] op_sel_hi:[0,1,1]
	v_pk_fma_f32 v[186:187], v[228:229], v[14:15], v[186:187] op_sel_hi:[0,1,1]
	s_waitcnt lgkmcnt(2)
	v_pk_fma_f32 v[186:187], v[192:193], v[16:17], v[186:187] op_sel_hi:[0,1,1]
	v_pk_fma_f32 v[186:187], v[192:193], v[18:19], v[186:187] op_sel:[1,0,0]
	v_mov_b32_e32 v188, v195
	v_pk_fma_f32 v[186:187], v[194:195], v[20:21], v[186:187] op_sel_hi:[0,1,1]
	v_pk_fma_f32 v[186:187], v[188:189], v[22:23], v[186:187] op_sel_hi:[0,1,1]
	s_waitcnt lgkmcnt(1)
	v_pk_fma_f32 v[186:187], v[196:197], v[24:25], v[186:187] op_sel_hi:[0,1,1]
	v_pk_fma_f32 v[186:187], v[196:197], v[26:27], v[186:187] op_sel:[1,0,0]
	v_mov_b32_e32 v188, v199
	v_pk_fma_f32 v[186:187], v[198:199], v[28:29], v[186:187] op_sel_hi:[0,1,1]
	v_pk_fma_f32 v[186:187], v[188:189], v[30:31], v[186:187] op_sel_hi:[0,1,1]
	s_waitcnt lgkmcnt(0)
	v_pk_fma_f32 v[186:187], v[222:223], v[32:33], v[186:187] op_sel_hi:[0,1,1]
	v_pk_fma_f32 v[192:193], v[222:223], v[34:35], v[186:187] op_sel:[1,0,0]
	ds_read_b128 v[186:189], v210 offset:57424
	v_pk_fma_f32 v[192:193], v[224:225], v[36:37], v[192:193] op_sel_hi:[0,1,1]
	v_mov_b32_e32 v194, v225
	v_pk_fma_f32 v[196:197], v[194:195], v[38:39], v[192:193] op_sel_hi:[0,1,1]
	ds_read_b128 v[192:195], v210 offset:57440
	s_waitcnt lgkmcnt(1)
	v_pk_fma_f32 v[196:197], v[186:187], v[40:41], v[196:197] op_sel_hi:[0,1,1]
	v_pk_fma_f32 v[186:187], v[186:187], v[42:43], v[196:197] op_sel:[1,0,0]
	s_nop 0
	v_pk_fma_f32 v[186:187], v[188:189], v[44:45], v[186:187] op_sel_hi:[0,1,1]
	v_mov_b32_e32 v188, v189
	v_pk_fma_f32 v[186:187], v[188:189], v[46:47], v[186:187] op_sel_hi:[0,1,1]
	s_waitcnt lgkmcnt(0)
	v_pk_fma_f32 v[186:187], v[192:193], v[48:49], v[186:187] op_sel_hi:[0,1,1]
	v_pk_fma_f32 v[192:193], v[192:193], v[50:51], v[186:187] op_sel:[1,0,0]
	ds_read_b128 v[186:189], v210 offset:57456
	v_pk_fma_f32 v[192:193], v[194:195], v[52:53], v[192:193] op_sel_hi:[0,1,1]
	v_mov_b32_e32 v194, v195
	v_pk_fma_f32 v[196:197], v[194:195], v[54:55], v[192:193] op_sel_hi:[0,1,1]
	ds_read_b128 v[192:195], v210 offset:57472
	s_waitcnt lgkmcnt(1)
	v_pk_fma_f32 v[196:197], v[186:187], v[56:57], v[196:197] op_sel_hi:[0,1,1]
	v_pk_fma_f32 v[186:187], v[186:187], v[58:59], v[196:197] op_sel:[1,0,0]
	s_nop 0
	v_pk_fma_f32 v[186:187], v[188:189], v[60:61], v[186:187] op_sel_hi:[0,1,1]
	v_mov_b32_e32 v188, v189
	v_pk_fma_f32 v[186:187], v[188:189], v[62:63], v[186:187] op_sel_hi:[0,1,1]
	s_waitcnt lgkmcnt(0)
	v_pk_fma_f32 v[186:187], v[192:193], v[64:65], v[186:187] op_sel_hi:[0,1,1]
	v_pk_fma_f32 v[186:187], v[192:193], v[66:67], v[186:187] op_sel:[1,0,0]
	v_mov_b32_e32 v188, v195
	v_pk_fma_f32 v[186:187], v[194:195], v[68:69], v[186:187] op_sel_hi:[0,1,1]
	v_pk_fma_f32 v[226:227], v[188:189], v[70:71], v[186:187] op_sel_hi:[0,1,1]
	ds_read_b128 v[186:189], v210 offset:57488
	ds_read_b128 v[192:195], v210 offset:57504
	ds_read_b128 v[196:199], v210 offset:57520
	ds_read_b128 v[222:225], v210 offset:57536
	s_waitcnt lgkmcnt(3)
	v_pk_fma_f32 v[226:227], v[186:187], v[72:73], v[226:227] op_sel_hi:[0,1,1]
	v_pk_fma_f32 v[186:187], v[186:187], v[74:75], v[226:227] op_sel:[1,0,0]
	v_mov_b32_e32 v228, v189
	v_pk_fma_f32 v[186:187], v[188:189], v[76:77], v[186:187] op_sel_hi:[0,1,1]
	v_pk_fma_f32 v[186:187], v[228:229], v[78:79], v[186:187] op_sel_hi:[0,1,1]
	s_waitcnt lgkmcnt(2)
; template <bool DRY = false>
; DI void phase_ln_router(const Params& p, char* smem, int bid, int nb) {
;     ...
;       for (int j = 0; j < 8; ++j) {
; #pragma unroll
;         for (int i4 = 0; i4 < 16; ++i4) {
;           const float4 h = *(const float4*)(hs + j * 2048 + ks * 64 + 4 * i4);
;           acc[j] = __builtin_elementwise_fma((f32x2_t){h.x, h.x}, wr[4 * i4], acc[j]); acc[j] = __builtin_elementwise_fma((f32x2_t){h.y, h.y}, wr[4 * i4 + 1], acc[j]);
;           acc[j] = __builtin_elementwise_fma((f32x2_t){h.z, h.z}, wr[4 * i4 + 2], acc[j]); acc[j] = __builtin_elementwise_fma((f32x2_t){h.w, h.w}, wr[4 * i4 + 3], acc[j]);
;           if ((i4 & 7) == 7) __builtin_amdgcn_sched_barrier(0);
;         }
;       }
; #pragma unroll
;       for (int j = 0; j < 8; ++j) { red[(ks * 8 + j) * 32 + e] = acc[j][0]; red[(ks * 8 + j) * 32 + e + 16] = acc[j][1]; }
;     }
;     __syncthreads();
;     if (tid < 256) {
;       const int e2 = tid & 31, j = tid >> 5;
;       float s = 0.f;
; #pragma unroll
;       for (int k2 = 0; k2 < 32; ++k2) s += red[(k2 * 8 + j) * 32 + e2];
;       lg[j * 32 + e2] = s + p.b_router[e2];
;     }
	v_pk_fma_f32 v[186:187], v[192:193], v[80:81], v[186:187] op_sel_hi:[0,1,1]
	v_pk_fma_f32 v[186:187], v[192:193], v[82:83], v[186:187] op_sel:[1,0,0]
	v_mov_b32_e32 v188, v195
	v_pk_fma_f32 v[186:187], v[194:195], v[84:85], v[186:187] op_sel_hi:[0,1,1]
	v_pk_fma_f32 v[186:187], v[188:189], v[86:87], v[186:187] op_sel_hi:[0,1,1]
	s_waitcnt lgkmcnt(1)
	v_pk_fma_f32 v[186:187], v[196:197], v[88:89], v[186:187] op_sel_hi:[0,1,1]
	v_pk_fma_f32 v[186:187], v[196:197], v[90:91], v[186:187] op_sel:[1,0,0]
	v_mov_b32_e32 v188, v199
	v_pk_fma_f32 v[186:187], v[198:199], v[92:93], v[186:187] op_sel_hi:[0,1,1]
	v_pk_fma_f32 v[186:187], v[188:189], v[94:95], v[186:187] op_sel_hi:[0,1,1]
	s_waitcnt lgkmcnt(0)
	v_pk_fma_f32 v[186:187], v[222:223], v[96:97], v[186:187] op_sel_hi:[0,1,1]
	v_pk_fma_f32 v[192:193], v[222:223], v[98:99], v[186:187] op_sel:[1,0,0]
	ds_read_b128 v[186:189], v210 offset:57552
	v_pk_fma_f32 v[192:193], v[224:225], v[100:101], v[192:193] op_sel_hi:[0,1,1]
	v_mov_b32_e32 v194, v225
	v_pk_fma_f32 v[196:197], v[194:195], v[102:103], v[192:193] op_sel_hi:[0,1,1]
	ds_read_b128 v[192:195], v210 offset:57568
	s_waitcnt lgkmcnt(1)
	v_pk_fma_f32 v[196:197], v[186:187], v[104:105], v[196:197] op_sel_hi:[0,1,1]
	v_pk_fma_f32 v[186:187], v[186:187], v[106:107], v[196:197] op_sel:[1,0,0]
	s_nop 0
	v_pk_fma_f32 v[186:187], v[188:189], v[108:109], v[186:187] op_sel_hi:[0,1,1]
	v_mov_b32_e32 v188, v189
	v_pk_fma_f32 v[186:187], v[188:189], v[110:111], v[186:187] op_sel_hi:[0,1,1]
	s_waitcnt lgkmcnt(0)
	v_pk_fma_f32 v[186:187], v[192:193], v[112:113], v[186:187] op_sel_hi:[0,1,1]
	v_pk_fma_f32 v[192:193], v[192:193], v[114:115], v[186:187] op_sel:[1,0,0]
	ds_read_b128 v[186:189], v210 offset:57584
	v_pk_fma_f32 v[192:193], v[194:195], v[116:117], v[192:193] op_sel_hi:[0,1,1]
	v_mov_b32_e32 v194, v195
	v_pk_fma_f32 v[196:197], v[194:195], v[118:119], v[192:193] op_sel_hi:[0,1,1]
	ds_read_b128 v[192:195], v210 offset:57600
	s_waitcnt lgkmcnt(1)
	v_pk_fma_f32 v[196:197], v[186:187], v[120:121], v[196:197] op_sel_hi:[0,1,1]
	v_pk_fma_f32 v[186:187], v[186:187], v[122:123], v[196:197] op_sel:[1,0,0]
	s_nop 0
	v_pk_fma_f32 v[186:187], v[188:189], v[124:125], v[186:187] op_sel_hi:[0,1,1]
	v_mov_b32_e32 v188, v189
	v_pk_fma_f32 v[186:187], v[188:189], v[126:127], v[186:187] op_sel_hi:[0,1,1]
	s_waitcnt lgkmcnt(0)
	v_pk_fma_f32 v[186:187], v[192:193], v[128:129], v[186:187] op_sel_hi:[0,1,1]
	v_pk_fma_f32 v[186:187], v[192:193], v[130:131], v[186:187] op_sel:[1,0,0]
	v_mov_b32_e32 v188, v195
	v_pk_fma_f32 v[186:187], v[194:195], v[132:133], v[186:187] op_sel_hi:[0,1,1]
	v_pk_fma_f32 v[186:187], v[188:189], v[134:135], v[186:187] op_sel_hi:[0,1,1]
	ds_write2_b32 v217, v0, v1 offset1:16
	ds_write2_b32 v217, v2, v3 offset0:32 offset1:48
	ds_write2_b32 v217, v4, v5 offset0:64 offset1:80
	ds_write2_b32 v217, v6, v7 offset0:96 offset1:112
	ds_write2_b32 v217, v182, v183 offset0:128 offset1:144
	ds_write2_b32 v217, v184, v185 offset0:160 offset1:176
	ds_write2_b32 v217, v190, v191 offset0:192 offset1:208
	ds_write2_b32 v217, v186, v187 offset0:224 offset1:240
	s_waitcnt lgkmcnt(0)
	s_barrier
	s_and_saveexec_b64 s[20:21], s[4:5]
	s_cbranch_execz .LBB0_1332
	global_load_dword v6, v[156:157], off
	ds_read2st64_b32 v[0:1], v211 offset1:4
	ds_read2st64_b32 v[2:3], v211 offset0:8 offset1:12
	ds_read2st64_b32 v[4:5], v211 offset0:16 offset1:20
	s_waitcnt lgkmcnt(2)
	v_add_f32_e32 v0, 0, v0
	v_add_f32_e32 v0, v0, v1
	s_waitcnt lgkmcnt(1)
	v_add_f32_e32 v2, v0, v2
	ds_read2st64_b32 v[0:1], v211 offset0:24 offset1:28
	v_add_f32_e32 v2, v2, v3
	s_waitcnt lgkmcnt(1)
	v_add_f32_e32 v4, v2, v4
	ds_read2st64_b32 v[2:3], v211 offset0:32 offset1:36
	v_add_f32_e32 v4, v4, v5
	s_waitcnt lgkmcnt(1)
	v_add_f32_e32 v0, v4, v0
	ds_read2st64_b32 v[4:5], v211 offset0:40 offset1:44
	v_add_f32_e32 v0, v0, v1
	s_waitcnt lgkmcnt(1)
	v_add_f32_e32 v2, v0, v2
	ds_read2st64_b32 v[0:1], v211 offset0:48 offset1:52
	v_add_f32_e32 v2, v2, v3
	s_waitcnt lgkmcnt(1)
	v_add_f32_e32 v4, v2, v4
	ds_read2st64_b32 v[2:3], v211 offset0:56 offset1:60
	v_add_f32_e32 v4, v4, v5
	s_waitcnt lgkmcnt(1)
	v_add_f32_e32 v0, v4, v0
	ds_read2st64_b32 v[4:5], v211 offset0:64 offset1:68
	v_add_f32_e32 v0, v0, v1
	s_waitcnt lgkmcnt(1)
	v_add_f32_e32 v2, v0, v2
	ds_read2st64_b32 v[0:1], v211 offset0:72 offset1:76
	v_add_f32_e32 v2, v2, v3
	s_waitcnt lgkmcnt(1)
	v_add_f32_e32 v4, v2, v4
	ds_read2st64_b32 v[2:3], v211 offset0:80 offset1:84
	v_add_f32_e32 v4, v4, v5
	s_waitcnt lgkmcnt(1)
	v_add_f32_e32 v0, v4, v0
	ds_read2st64_b32 v[4:5], v211 offset0:88 offset1:92
	v_add_f32_e32 v0, v0, v1
	s_waitcnt lgkmcnt(1)
	v_add_f32_e32 v2, v0, v2
	ds_read2st64_b32 v[0:1], v211 offset0:96 offset1:100
	v_add_f32_e32 v2, v2, v3
	s_waitcnt lgkmcnt(1)
	v_add_f32_e32 v2, v2, v4
	v_add_f32_e32 v4, v2, v5
	ds_read2st64_b32 v[2:3], v211 offset0:104 offset1:108
	s_waitcnt lgkmcnt(1)
	v_add_f32_e32 v0, v4, v0
	ds_read2st64_b32 v[4:5], v211 offset0:112 offset1:116
	v_add_f32_e32 v7, v0, v1
	ds_read2st64_b32 v[0:1], v211 offset0:120 offset1:124
	s_waitcnt lgkmcnt(2)
	v_add_f32_e32 v2, v7, v2
	v_add_f32_e32 v2, v2, v3
	s_waitcnt lgkmcnt(1)
	v_add_f32_e32 v2, v2, v4
	v_add_f32_e32 v2, v2, v5
	s_waitcnt lgkmcnt(0)
	v_add_f32_e32 v0, v2, v0
	v_add_f32_e32 v0, v0, v1
	s_waitcnt vmcnt(0)
	v_add_f32_e32 v0, v0, v6
	ds_write_b32 v212, v0
